# K-loop MFMA segments: one priority raise per segment (the s_setprio 0 / s_setprio 1 pair between the two MFMA blocks removed, 28 sites)
# speedup vs baseline: 1.0103x; 1.0062x over previous
; #define PG8_STAGE(bufoff, gbase, voff) do { _Pragma("unroll") for (int _i = 0; _i < 2; ++_i) \
;         __builtin_amdgcn_global_load_lds((const unsigned*)((const char*)(gbase) + (voff)[_i]), (PG8_LAS unsigned*)(lds + (bufoff) + ldsw + _i * 8192), 16, 0, 0); } while (0)
; #define PG8_LDA(dst, b, h) do { _Pragma("unroll") for (int m = 0; m < 4; ++m) { const bf16x8 f0_ = *(const PG8_LAS bf16x8*)(lds + PG8_SA(b, h) + aoff + m * 2048), f1_ = *(const PG8_LAS bf16x8*)(lds + PG8_SA(b, h) + aoff + m * 2048 + 1024); dst[m].set(f0_, f1_); } } while (0)
; #define PG8_LDB(dst, b, h) do { _Pragma("unroll") for (int n = 0; n < 2; ++n) { const bf16x8 f0_ = *(const PG8_LAS bf16x8*)(lds + PG8_SB(b, h) + boff + n * 2048), f1_ = *(const PG8_LAS bf16x8*)(lds + PG8_SB(b, h) + boff + n * 2048 + 1024); dst[n].set(f0_, f1_); } } while (0)
; #define PG8_WAIT_V(n) asm volatile("s_waitcnt vmcnt(" #n ")" ::: "memory")
; #define PG8_WAIT_L(n) asm volatile("s_waitcnt lgkmcnt(" #n ")" ::: "memory")
; #define PG8_BAR __builtin_amdgcn_s_barrier()
; #define PG8_SCHED __builtin_amdgcn_sched_barrier(0)
; template <class Epi, class Sched, bool ALIGN_EPI = false, bool SP2 = false>
; __device__ __forceinline__ void gemm_phase(PG8_LAS unsigned char* lds, const Gemm g, const Sched& S, const Epi& E) {
;     ...
;             PG8_LDB(B0, 0, 0); PG8_LDB(B1, 0, 1); PG8_SCHED; PG8_LDA(At, 0, 0); PG8_STAGE(PG8_SA(1, 1), a1 + hstep, voffA);
;             PG8_WAIT_V(8); PG8_WAIT_L(0); PG8_BAR; PG8_MMA(0, 0, At, B0); PG8_MMA(0, 1, At, B1); PG8_BAR; PG8_SCHED;
;             PG8_LDA(At, 0, 1); PG8_STAGE(PG8_SB(0, 0), b2, voffB); PG8_STAGE(PG8_SB(0, 1), b2 + hstepB, voffB); PG8_STAGE(PG8_SA(0, 0), a2, voffA);
;             PG8_WAIT_V(8); PG8_WAIT_L(0); PG8_BAR; PG8_MMA(1, 0, At, B0); PG8_MMA(1, 1, At, B1); PG8_BAR; PG8_SCHED;
.Lkr0_a:
	v_lshl_add_u64 v[190:191], s[2:3], 0, v[174:175]
	s_add_i32 m0, s58, 0xc000
	ds_read_b128 v[182:185], v205
	ds_read_b128 v[186:189], v205 offset:1024
	ds_read_b128 v[212:215], v205 offset:2048
	ds_read_b128 v[216:219], v205 offset:3072
	ds_read_b128 v[220:223], v205 offset:4096
	ds_read_b128 v[224:227], v205 offset:5120
	ds_read_b128 v[228:231], v205 offset:6144
	ds_read_b128 v[232:235], v205 offset:7168
	global_load_lds_dwordx4 v[190:191], off
	v_lshl_add_u64 v[190:191], s[2:3], 0, v[176:177]
	s_add_i32 m0, s58, 0xe000
	s_nop 0
	global_load_lds_dwordx4 v[190:191], off
	s_waitcnt vmcnt(8)
	s_waitcnt lgkmcnt(0)
	s_barrier
	s_setprio 1
	s_waitcnt lgkmcnt(0)
	v_mfma_scale_f32_16x16x128_f8f6f4 v[158:161], v[18:25], v[182:189], v[158:161], v206, v207 op_sel_hi:[0,0,0]
	v_mfma_scale_f32_16x16x128_f8f6f4 v[154:157], v[26:33], v[182:189], v[154:157], v206, v207 op_sel_hi:[0,0,0]
	v_mfma_scale_f32_16x16x128_f8f6f4 v[142:145], v[18:25], v[212:219], v[142:145], v206, v207 op_sel_hi:[0,0,0]
	v_mfma_scale_f32_16x16x128_f8f6f4 v[138:141], v[26:33], v[212:219], v[138:141], v206, v207 op_sel_hi:[0,0,0]
	v_mfma_scale_f32_16x16x128_f8f6f4 v[126:129], v[18:25], v[220:227], v[126:129], v206, v207 op_sel_hi:[0,0,0]
	v_mfma_scale_f32_16x16x128_f8f6f4 v[122:125], v[26:33], v[220:227], v[122:125], v206, v207 op_sel_hi:[0,0,0]
	v_mfma_scale_f32_16x16x128_f8f6f4 v[110:113], v[18:25], v[228:235], v[110:113], v206, v207 op_sel_hi:[0,0,0]
	v_mfma_scale_f32_16x16x128_f8f6f4 v[106:109], v[26:33], v[228:235], v[106:109], v206, v207 op_sel_hi:[0,0,0]
	v_mfma_scale_f32_16x16x128_f8f6f4 v[150:153], v[2:9], v[182:189], v[150:153], v206, v207 op_sel_hi:[0,0,0]
	v_mfma_scale_f32_16x16x128_f8f6f4 v[146:149], v[10:17], v[182:189], v[146:149], v206, v207 op_sel_hi:[0,0,0]
	v_mfma_scale_f32_16x16x128_f8f6f4 v[134:137], v[2:9], v[212:219], v[134:137], v206, v207 op_sel_hi:[0,0,0]
	v_mfma_scale_f32_16x16x128_f8f6f4 v[130:133], v[10:17], v[212:219], v[130:133], v206, v207 op_sel_hi:[0,0,0]
	v_mfma_scale_f32_16x16x128_f8f6f4 v[118:121], v[2:9], v[220:227], v[118:121], v206, v207 op_sel_hi:[0,0,0]
	v_mfma_scale_f32_16x16x128_f8f6f4 v[114:117], v[10:17], v[220:227], v[114:117], v206, v207 op_sel_hi:[0,0,0]
	v_mfma_scale_f32_16x16x128_f8f6f4 v[102:105], v[2:9], v[228:235], v[102:105], v206, v207 op_sel_hi:[0,0,0]
	v_mfma_scale_f32_16x16x128_f8f6f4 v[98:101], v[10:17], v[228:235], v[98:101], v206, v207 op_sel_hi:[0,0,0]
	s_setprio 0
	s_barrier
	s_add_i32 s0, s76, s57
	v_lshl_add_u64 v[182:183], s[50:51], 0, v[164:165]
	s_mov_b32 m0, s0
	ds_read_b128 v[212:215], v205 offset:16384
	ds_read_b128 v[216:219], v205 offset:17408
	ds_read_b128 v[220:223], v205 offset:18432
	ds_read_b128 v[224:227], v205 offset:19456
	ds_read_b128 v[228:231], v205 offset:20480
	ds_read_b128 v[232:235], v205 offset:21504
	ds_read_b128 v[236:239], v205 offset:22528
	ds_read_b128 v[240:243], v205 offset:23552
	global_load_lds_dwordx4 v[182:183], off
	s_add_i32 m0, s0, 0x2000
	v_lshl_add_u64 v[184:185], s[50:51], 0, v[168:169]
	s_add_u32 s50, s50, s16
	s_addc_u32 s51, s51, s17
	s_add_i32 s0, s77, s57
	global_load_lds_dwordx4 v[184:185], off
	v_lshl_add_u64 v[186:187], s[50:51], 0, v[164:165]
	s_mov_b32 m0, s0
	v_lshl_add_u64 v[188:189], s[50:51], 0, v[168:169]
	global_load_lds_dwordx4 v[186:187], off
	s_add_i32 m0, s0, 0x2000
	v_lshl_add_u64 v[190:191], s[48:49], 0, v[162:163]
	global_load_lds_dwordx4 v[188:189], off
	v_lshl_add_u64 v[192:193], s[48:49], 0, v[166:167]
	s_waitcnt vmcnt(6)
	s_waitcnt lgkmcnt(0)
	s_barrier
	s_setprio 1
	s_waitcnt lgkmcnt(0)
	v_mfma_scale_f32_16x16x128_f8f6f4 v[94:97], v[18:25], v[212:219], v[94:97], v206, v207 op_sel_hi:[0,0,0]
	v_mfma_scale_f32_16x16x128_f8f6f4 v[90:93], v[26:33], v[212:219], v[90:93], v206, v207 op_sel_hi:[0,0,0]
	v_mfma_scale_f32_16x16x128_f8f6f4 v[78:81], v[18:25], v[220:227], v[78:81], v206, v207 op_sel_hi:[0,0,0]
	v_mfma_scale_f32_16x16x128_f8f6f4 v[74:77], v[26:33], v[220:227], v[74:77], v206, v207 op_sel_hi:[0,0,0]
	v_mfma_scale_f32_16x16x128_f8f6f4 v[62:65], v[18:25], v[228:235], v[62:65], v206, v207 op_sel_hi:[0,0,0]
	v_mfma_scale_f32_16x16x128_f8f6f4 v[58:61], v[26:33], v[228:235], v[58:61], v206, v207 op_sel_hi:[0,0,0]
	v_mfma_scale_f32_16x16x128_f8f6f4 v[46:49], v[18:25], v[236:243], v[46:49], v206, v207 op_sel_hi:[0,0,0]
	v_mfma_scale_f32_16x16x128_f8f6f4 v[42:45], v[26:33], v[236:243], v[42:45], v206, v207 op_sel_hi:[0,0,0]
	v_mfma_scale_f32_16x16x128_f8f6f4 v[86:89], v[2:9], v[212:219], v[86:89], v206, v207 op_sel_hi:[0,0,0]
	v_mfma_scale_f32_16x16x128_f8f6f4 v[82:85], v[10:17], v[212:219], v[82:85], v206, v207 op_sel_hi:[0,0,0]
	v_mfma_scale_f32_16x16x128_f8f6f4 v[70:73], v[2:9], v[220:227], v[70:73], v206, v207 op_sel_hi:[0,0,0]
	v_mfma_scale_f32_16x16x128_f8f6f4 v[66:69], v[10:17], v[220:227], v[66:69], v206, v207 op_sel_hi:[0,0,0]
	v_mfma_scale_f32_16x16x128_f8f6f4 v[54:57], v[2:9], v[228:235], v[54:57], v206, v207 op_sel_hi:[0,0,0]
	v_mfma_scale_f32_16x16x128_f8f6f4 v[50:53], v[10:17], v[228:235], v[50:53], v206, v207 op_sel_hi:[0,0,0]
	v_mfma_scale_f32_16x16x128_f8f6f4 v[38:41], v[2:9], v[236:243], v[38:41], v206, v207 op_sel_hi:[0,0,0]
	v_mfma_scale_f32_16x16x128_f8f6f4 v[34:37], v[10:17], v[236:243], v[34:37], v206, v207 op_sel_hi:[0,0,0]
	s_setprio 0
	s_barrier
; #define PG8_STAGE(bufoff, gbase, voff) do { _Pragma("unroll") for (int _i = 0; _i < 2; ++_i) \
;         __builtin_amdgcn_global_load_lds((const unsigned*)((const char*)(gbase) + (voff)[_i]), (PG8_LAS unsigned*)(lds + (bufoff) + ldsw + _i * 8192), 16, 0, 0); } while (0)
; #define PG8_LDA(dst, b, h) do { _Pragma("unroll") for (int m = 0; m < 4; ++m) { const bf16x8 f0_ = *(const PG8_LAS bf16x8*)(lds + PG8_SA(b, h) + aoff + m * 2048), f1_ = *(const PG8_LAS bf16x8*)(lds + PG8_SA(b, h) + aoff + m * 2048 + 1024); dst[m].set(f0_, f1_); } } while (0)
; #define PG8_LDB(dst, b, h) do { _Pragma("unroll") for (int n = 0; n < 2; ++n) { const bf16x8 f0_ = *(const PG8_LAS bf16x8*)(lds + PG8_SB(b, h) + boff + n * 2048), f1_ = *(const PG8_LAS bf16x8*)(lds + PG8_SB(b, h) + boff + n * 2048 + 1024); dst[n].set(f0_, f1_); } } while (0)
; #define PG8_WAIT_V(n) asm volatile("s_waitcnt vmcnt(" #n ")" ::: "memory")
; #define PG8_WAIT_L(n) asm volatile("s_waitcnt lgkmcnt(" #n ")" ::: "memory")
; #define PG8_BAR __builtin_amdgcn_s_barrier()
; #define PG8_SCHED __builtin_amdgcn_sched_barrier(0)
; template <class Epi, class Sched, bool ALIGN_EPI = false, bool SP2 = false>
; __device__ __forceinline__ void gemm_phase(PG8_LAS unsigned char* lds, const Gemm g, const Sched& S, const Epi& E) {
;     ...
;             PG8_LDB(B0, 1, 0); PG8_LDB(B1, 1, 1); PG8_SCHED; PG8_LDA(At, 1, 0); PG8_STAGE(PG8_SA(0, 1), a2 + hstep, voffA);
;             PG8_WAIT_V(8); PG8_WAIT_L(0); PG8_BAR; PG8_MMA(0, 0, At, B0); PG8_MMA(0, 1, At, B1); PG8_BAR; PG8_SCHED;
;             PG8_LDA(At, 1, 1); PG8_STAGE(PG8_SB(1, 0), b3, voffB); PG8_STAGE(PG8_SB(1, 1), b3 + hstepB, voffB); PG8_STAGE(PG8_SA(1, 0), a3, voffA);
;             PG8_WAIT_V(8); PG8_WAIT_L(0); PG8_BAR; PG8_MMA(1, 0, At, B0); PG8_MMA(1, 1, At, B1); PG8_BAR; PG8_SCHED;
	s_add_i32 s0, 0, 0x18000
	s_add_i32 s1, 0, 0x1c000
	v_add_u32_e32 v14, s0, v194
	v_add_u32_e32 v30, s1, v194
	ds_read_b128 v[2:5], v14
	ds_read_b128 v[6:9], v14 offset:1024
	ds_read_b128 v[10:13], v14 offset:2048
	ds_read_b128 v[14:17], v14 offset:3072
	ds_read_b128 v[18:21], v30
	ds_read_b128 v[22:25], v30 offset:1024
	ds_read_b128 v[26:29], v30 offset:2048
	ds_read_b128 v[30:33], v30 offset:3072
	s_add_u32 s48, s48, s14
	s_addc_u32 s49, s49, s15
	s_mov_b32 m0, s61
	v_lshl_add_u64 v[244:245], s[48:49], 0, v[162:163]
	ds_read_b128 v[212:215], v205 offset:32768
	ds_read_b128 v[216:219], v205 offset:33792
	ds_read_b128 v[220:223], v205 offset:34816
	ds_read_b128 v[224:227], v205 offset:35840
	ds_read_b128 v[228:231], v205 offset:36864
	ds_read_b128 v[232:235], v205 offset:37888
	ds_read_b128 v[236:239], v205 offset:38912
	ds_read_b128 v[240:243], v205 offset:39936
	s_mov_b32 m0, s58
	s_nop 0
	global_load_lds_dwordx4 v[190:191], off
	s_mov_b32 m0, s59
	s_nop 0
	global_load_lds_dwordx4 v[192:193], off
	s_mov_b32 m0, s61
	s_nop 0
	global_load_lds_dwordx4 v[244:245], off
	v_lshl_add_u64 v[244:245], s[48:49], 0, v[166:167]
	s_mov_b32 m0, s63
	s_nop 0
	global_load_lds_dwordx4 v[244:245], off
	s_waitcnt vmcnt(8)
	s_waitcnt lgkmcnt(0)
	s_barrier
	s_setprio 1
	s_waitcnt lgkmcnt(0)
	v_mfma_scale_f32_16x16x128_f8f6f4 v[158:161], v[2:9], v[212:219], v[158:161], v206, v207 op_sel_hi:[0,0,0]
	v_mfma_scale_f32_16x16x128_f8f6f4 v[154:157], v[10:17], v[212:219], v[154:157], v206, v207 op_sel_hi:[0,0,0]
	v_mfma_scale_f32_16x16x128_f8f6f4 v[142:145], v[2:9], v[220:227], v[142:145], v206, v207 op_sel_hi:[0,0,0]
	v_mfma_scale_f32_16x16x128_f8f6f4 v[138:141], v[10:17], v[220:227], v[138:141], v206, v207 op_sel_hi:[0,0,0]
	v_mfma_scale_f32_16x16x128_f8f6f4 v[126:129], v[2:9], v[228:235], v[126:129], v206, v207 op_sel_hi:[0,0,0]
	v_mfma_scale_f32_16x16x128_f8f6f4 v[122:125], v[10:17], v[228:235], v[122:125], v206, v207 op_sel_hi:[0,0,0]
	v_mfma_scale_f32_16x16x128_f8f6f4 v[110:113], v[2:9], v[236:243], v[110:113], v206, v207 op_sel_hi:[0,0,0]
	v_mfma_scale_f32_16x16x128_f8f6f4 v[106:109], v[10:17], v[236:243], v[106:109], v206, v207 op_sel_hi:[0,0,0]
	v_mfma_scale_f32_16x16x128_f8f6f4 v[150:153], v[18:25], v[212:219], v[150:153], v206, v207 op_sel_hi:[0,0,0]
	v_mfma_scale_f32_16x16x128_f8f6f4 v[146:149], v[26:33], v[212:219], v[146:149], v206, v207 op_sel_hi:[0,0,0]
	v_mfma_scale_f32_16x16x128_f8f6f4 v[134:137], v[18:25], v[220:227], v[134:137], v206, v207 op_sel_hi:[0,0,0]
	v_mfma_scale_f32_16x16x128_f8f6f4 v[130:133], v[26:33], v[220:227], v[130:133], v206, v207 op_sel_hi:[0,0,0]
	v_mfma_scale_f32_16x16x128_f8f6f4 v[118:121], v[18:25], v[228:235], v[118:121], v206, v207 op_sel_hi:[0,0,0]
	v_mfma_scale_f32_16x16x128_f8f6f4 v[114:117], v[26:33], v[228:235], v[114:117], v206, v207 op_sel_hi:[0,0,0]
	v_mfma_scale_f32_16x16x128_f8f6f4 v[102:105], v[18:25], v[236:243], v[102:105], v206, v207 op_sel_hi:[0,0,0]
	v_mfma_scale_f32_16x16x128_f8f6f4 v[98:101], v[26:33], v[236:243], v[98:101], v206, v207 op_sel_hi:[0,0,0]
	s_setprio 0
	s_barrier
	s_add_i32 s0, s0, s57
	v_lshl_add_u64 v[182:183], v[182:183], 0, s[36:37]
	s_mov_b32 m0, s0
	ds_read_b128 v[212:215], v205 offset:49152
	ds_read_b128 v[216:219], v205 offset:50176
	ds_read_b128 v[220:223], v205 offset:51200
	ds_read_b128 v[224:227], v205 offset:52224
	ds_read_b128 v[228:231], v205 offset:53248
	ds_read_b128 v[232:235], v205 offset:54272
	ds_read_b128 v[236:239], v205 offset:55296
	ds_read_b128 v[240:243], v205 offset:56320
	global_load_lds_dwordx4 v[182:183], off
	v_lshl_add_u64 v[182:183], v[184:185], 0, s[36:37]
	s_add_i32 m0, s0, 0x2000
	s_add_i32 s0, s1, s57
	global_load_lds_dwordx4 v[182:183], off
	v_lshl_add_u64 v[182:183], v[186:187], 0, s[36:37]
	s_mov_b32 m0, s0
	s_nop 0
	global_load_lds_dwordx4 v[182:183], off
	v_lshl_add_u64 v[182:183], v[188:189], 0, s[36:37]
	s_add_i32 m0, s0, 0x2000
	s_nop 0
	global_load_lds_dwordx4 v[182:183], off
	s_cmp_ge_i32 s53, s69
	s_cbranch_scc0 .Lkr0_b
	v_lshl_add_u64 v[182:183], v[190:191], 0, s[36:37]
	s_mov_b32 m0, s66
	s_nop 0
	global_load_lds_dwordx4 v[182:183], off
	v_lshl_add_u64 v[182:183], v[192:193], 0, s[36:37]
	s_mov_b32 m0, s67
	s_nop 0
	global_load_lds_dwordx4 v[182:183], off
.Lkr0_b:
	s_waitcnt vmcnt(6)
	s_waitcnt lgkmcnt(0)
	s_barrier
	s_setprio 1
	s_waitcnt lgkmcnt(0)
	v_mfma_scale_f32_16x16x128_f8f6f4 v[94:97], v[2:9], v[212:219], v[94:97], v206, v207 op_sel_hi:[0,0,0]
	v_mfma_scale_f32_16x16x128_f8f6f4 v[90:93], v[10:17], v[212:219], v[90:93], v206, v207 op_sel_hi:[0,0,0]
	v_mfma_scale_f32_16x16x128_f8f6f4 v[78:81], v[2:9], v[220:227], v[78:81], v206, v207 op_sel_hi:[0,0,0]
	v_mfma_scale_f32_16x16x128_f8f6f4 v[74:77], v[10:17], v[220:227], v[74:77], v206, v207 op_sel_hi:[0,0,0]
	v_mfma_scale_f32_16x16x128_f8f6f4 v[62:65], v[2:9], v[228:235], v[62:65], v206, v207 op_sel_hi:[0,0,0]
	v_mfma_scale_f32_16x16x128_f8f6f4 v[58:61], v[10:17], v[228:235], v[58:61], v206, v207 op_sel_hi:[0,0,0]
	v_mfma_scale_f32_16x16x128_f8f6f4 v[46:49], v[2:9], v[236:243], v[46:49], v206, v207 op_sel_hi:[0,0,0]
	v_mfma_scale_f32_16x16x128_f8f6f4 v[42:45], v[10:17], v[236:243], v[42:45], v206, v207 op_sel_hi:[0,0,0]
	v_mfma_scale_f32_16x16x128_f8f6f4 v[86:89], v[18:25], v[212:219], v[86:89], v206, v207 op_sel_hi:[0,0,0]
	v_mfma_scale_f32_16x16x128_f8f6f4 v[82:85], v[26:33], v[212:219], v[82:85], v206, v207 op_sel_hi:[0,0,0]
	v_mfma_scale_f32_16x16x128_f8f6f4 v[70:73], v[18:25], v[220:227], v[70:73], v206, v207 op_sel_hi:[0,0,0]
	v_mfma_scale_f32_16x16x128_f8f6f4 v[66:69], v[26:33], v[220:227], v[66:69], v206, v207 op_sel_hi:[0,0,0]
	v_mfma_scale_f32_16x16x128_f8f6f4 v[54:57], v[18:25], v[228:235], v[54:57], v206, v207 op_sel_hi:[0,0,0]
	v_mfma_scale_f32_16x16x128_f8f6f4 v[50:53], v[26:33], v[228:235], v[50:53], v206, v207 op_sel_hi:[0,0,0]
	v_mfma_scale_f32_16x16x128_f8f6f4 v[38:41], v[18:25], v[236:243], v[38:41], v206, v207 op_sel_hi:[0,0,0]
	v_mfma_scale_f32_16x16x128_f8f6f4 v[34:37], v[26:33], v[236:243], v[34:37], v206, v207 op_sel_hi:[0,0,0]
	s_setprio 0
	s_barrier
	s_add_u32 s2, s2, 0x100
	s_addc_u32 s3, s3, 0
	s_add_u32 s20, s20, 0x100
	s_addc_u32 s52, s52, 0
	s_cmp_ge_i32 s53, s69
	s_cselect_b32 s99, 0, 1
	s_mov_b32 s48, s53
	s_cbranch_scc0 .LBB0_204

; #define PG8_STAGE(bufoff, gbase, voff) do { _Pragma("unroll") for (int _i = 0; _i < 2; ++_i) \
;         __builtin_amdgcn_global_load_lds((const unsigned*)((const char*)(gbase) + (voff)[_i]), (PG8_LAS unsigned*)(lds + (bufoff) + ldsw + _i * 8192), 16, 0, 0); } while (0)
; #define PG8_LDA(dst, b, h) do { _Pragma("unroll") for (int m = 0; m < 4; ++m) { const bf16x8 f0_ = *(const PG8_LAS bf16x8*)(lds + PG8_SA(b, h) + aoff + m * 2048), f1_ = *(const PG8_LAS bf16x8*)(lds + PG8_SA(b, h) + aoff + m * 2048 + 1024); dst[m].set(f0_, f1_); } } while (0)
; #define PG8_LDB(dst, b, h) do { _Pragma("unroll") for (int n = 0; n < 2; ++n) { const bf16x8 f0_ = *(const PG8_LAS bf16x8*)(lds + PG8_SB(b, h) + boff + n * 2048), f1_ = *(const PG8_LAS bf16x8*)(lds + PG8_SB(b, h) + boff + n * 2048 + 1024); dst[n].set(f0_, f1_); } } while (0)
; #define PG8_WAIT_V(n) asm volatile("s_waitcnt vmcnt(" #n ")" ::: "memory")
; #define PG8_WAIT_L(n) asm volatile("s_waitcnt lgkmcnt(" #n ")" ::: "memory")
; #define PG8_BAR __builtin_amdgcn_s_barrier()
; #define PG8_SCHED __builtin_amdgcn_sched_barrier(0)
; template <class Epi, class Sched, bool ALIGN_EPI = false, bool SP2 = false>
; __device__ __forceinline__ void gemm_phase(PG8_LAS unsigned char* lds, const Gemm g, const Sched& S, const Epi& E) {
;     ...
;             const bool last = (t == nt - 2);
;             const char* a1 = cA + (size_t)(t + 1) * kstep;
;             const char* a2 = last ? nA : cA + (size_t)(t + 2) * kstep; const char* b2 = last ? nB : cB + (size_t)(t + 2) * kstep;
;             const char* a3 = a2 + kstep; const char* b3 = b2 + kstep;
;             if (last && has_next) S.a_ready(nxt);
;             if constexpr (SP2) {
;             PG8_LDB(B0, 0, 0); PG8_LDB(B1, 0, 1); PG8_SCHED; PG8_LDA(At, 0, 0); PG8_STAGE(PG8_SA(1, 1), a1 + hstep, voffA);
;             PG8_WAIT_V(8); PG8_WAIT_L(0); PG8_BAR; PG8_MMA(0, 0, At, B0); PG8_MMA(0, 1, At, B1); PG8_BAR; PG8_SCHED;
;             PG8_LDA(At, 0, 1); PG8_STAGE(PG8_SB(0, 0), b2, voffB); PG8_STAGE(PG8_SB(0, 1), b2 + hstepB, voffB); PG8_STAGE(PG8_SA(0, 0), a2, voffA);
;             PG8_WAIT_V(8); PG8_WAIT_L(0); PG8_BAR; PG8_MMA(1, 0, At, B0); PG8_MMA(1, 1, At, B1); PG8_BAR; PG8_SCHED;
.LBB0_984:
	s_add_i32 s75, s42, 2
	v_add_u32_e32 v186, s59, v173
	v_add_u32_e32 v202, s61, v173
	s_add_u32 s0, s38, s40
	ds_read_b128 v[168:171], v186
	ds_read_b128 v[178:181], v186 offset:1024
	ds_read_b128 v[182:185], v186 offset:2048
	ds_read_b128 v[186:189], v186 offset:3072
	ds_read_b128 v[190:193], v202
	ds_read_b128 v[194:197], v202 offset:1024
	ds_read_b128 v[198:201], v202 offset:2048
	ds_read_b128 v[202:205], v202 offset:3072
	s_addc_u32 s1, s39, s41
	s_add_u32 s0, s0, 0x100
	s_addc_u32 s1, s1, 0
	s_add_u32 s33, s73, s40
	s_addc_u32 s76, s74, s41
	s_cmp_eq_u32 s57, s42
	s_cselect_b32 s43, s3, s1
	s_cselect_b32 s42, s2, s0
	s_cselect_b32 s1, s37, s76
	s_cselect_b32 s0, s36, s33
	v_lshl_add_u64 v[240:241], v[164:165], 0, s[40:41]
	s_add_i32 m0, s47, 0xc000
	ds_read_b128 v[206:209], v176
	ds_read_b128 v[212:215], v176 offset:1024
	ds_read_b128 v[216:219], v176 offset:2048
	ds_read_b128 v[220:223], v176 offset:3072
	ds_read_b128 v[224:227], v176 offset:4096
	ds_read_b128 v[228:231], v176 offset:5120
	ds_read_b128 v[232:235], v176 offset:6144
	ds_read_b128 v[236:239], v176 offset:7168
	global_load_lds_dwordx4 v[240:241], off
	v_lshl_add_u64 v[240:241], v[166:167], 0, s[40:41]
	s_add_i32 m0, s47, 0xe000
	s_nop 0
	global_load_lds_dwordx4 v[240:241], off
	s_waitcnt vmcnt(8)
	s_waitcnt lgkmcnt(0)
	s_barrier
	s_setprio 1
	s_waitcnt lgkmcnt(0)
	v_mfma_f32_16x16x32_bf16 v[126:129], v[168:171], v[206:209], v[126:129]
	v_mfma_f32_16x16x32_bf16 v[122:125], v[182:185], v[206:209], v[122:125]
	v_mfma_f32_16x16x32_bf16 v[110:113], v[168:171], v[216:219], v[110:113]
	v_mfma_f32_16x16x32_bf16 v[106:109], v[182:185], v[216:219], v[106:109]
	v_mfma_f32_16x16x32_bf16 v[94:97], v[168:171], v[224:227], v[94:97]
	v_mfma_f32_16x16x32_bf16 v[90:93], v[182:185], v[224:227], v[90:93]
	v_mfma_f32_16x16x32_bf16 v[78:81], v[168:171], v[232:235], v[78:81]
	v_mfma_f32_16x16x32_bf16 v[74:77], v[182:185], v[232:235], v[74:77]
	v_mfma_f32_16x16x32_bf16 v[126:129], v[178:181], v[212:215], v[126:129]
	v_mfma_f32_16x16x32_bf16 v[122:125], v[186:189], v[212:215], v[122:125]
	v_mfma_f32_16x16x32_bf16 v[110:113], v[178:181], v[220:223], v[110:113]
	v_mfma_f32_16x16x32_bf16 v[106:109], v[186:189], v[220:223], v[106:109]
	v_mfma_f32_16x16x32_bf16 v[94:97], v[178:181], v[228:231], v[94:97]
	v_mfma_f32_16x16x32_bf16 v[90:93], v[186:189], v[228:231], v[90:93]
	v_mfma_f32_16x16x32_bf16 v[78:81], v[178:181], v[236:239], v[78:81]
	v_mfma_f32_16x16x32_bf16 v[74:77], v[186:189], v[236:239], v[74:77]
	v_mfma_f32_16x16x32_bf16 v[118:121], v[190:193], v[206:209], v[118:121]
	v_mfma_f32_16x16x32_bf16 v[114:117], v[198:201], v[206:209], v[114:117]
	v_mfma_f32_16x16x32_bf16 v[102:105], v[190:193], v[216:219], v[102:105]
	v_mfma_f32_16x16x32_bf16 v[98:101], v[198:201], v[216:219], v[98:101]
	v_mfma_f32_16x16x32_bf16 v[86:89], v[190:193], v[224:227], v[86:89]
	v_mfma_f32_16x16x32_bf16 v[82:85], v[198:201], v[224:227], v[82:85]
	v_mfma_f32_16x16x32_bf16 v[70:73], v[190:193], v[232:235], v[70:73]
	v_mfma_f32_16x16x32_bf16 v[66:69], v[198:201], v[232:235], v[66:69]
	v_mfma_f32_16x16x32_bf16 v[118:121], v[194:197], v[212:215], v[118:121]
	v_mfma_f32_16x16x32_bf16 v[114:117], v[202:205], v[212:215], v[114:117]
	v_mfma_f32_16x16x32_bf16 v[102:105], v[194:197], v[220:223], v[102:105]
	v_mfma_f32_16x16x32_bf16 v[98:101], v[202:205], v[220:223], v[98:101]
	v_mfma_f32_16x16x32_bf16 v[86:89], v[194:197], v[228:231], v[86:89]
	v_mfma_f32_16x16x32_bf16 v[82:85], v[202:205], v[228:231], v[82:85]
	v_mfma_f32_16x16x32_bf16 v[70:73], v[194:197], v[236:239], v[70:73]
	v_mfma_f32_16x16x32_bf16 v[66:69], v[202:205], v[236:239], v[66:69]
	s_setprio 0
	s_barrier
	s_add_i32 s33, s59, s46
	v_lshl_add_u64 v[240:241], s[0:1], 0, v[132:133]
	s_mov_b32 m0, s33
	ds_read_b128 v[206:209], v176 offset:16384
	ds_read_b128 v[212:215], v176 offset:17408
	ds_read_b128 v[216:219], v176 offset:18432
	ds_read_b128 v[220:223], v176 offset:19456
	ds_read_b128 v[224:227], v176 offset:20480
	ds_read_b128 v[228:231], v176 offset:21504
	ds_read_b128 v[232:235], v176 offset:22528
	ds_read_b128 v[236:239], v176 offset:23552
	global_load_lds_dwordx4 v[240:241], off
	s_add_i32 m0, s33, 0x2000
	v_lshl_add_u64 v[242:243], s[0:1], 0, v[136:137]
	s_add_u32 s0, s0, s14
	s_addc_u32 s1, s1, s15
	s_add_i32 s33, s61, s46
	global_load_lds_dwordx4 v[242:243], off
	v_lshl_add_u64 v[244:245], s[0:1], 0, v[132:133]
	s_mov_b32 m0, s33
	v_lshl_add_u64 v[246:247], s[0:1], 0, v[136:137]
	global_load_lds_dwordx4 v[244:245], off
	s_add_i32 m0, s33, 0x2000
	v_lshl_add_u64 v[248:249], s[42:43], 0, v[130:131]
	global_load_lds_dwordx4 v[246:247], off
	v_lshl_add_u64 v[250:251], s[42:43], 0, v[134:135]
	s_waitcnt vmcnt(6)
	s_waitcnt lgkmcnt(0)
	s_barrier
; #define PG8_STAGE(bufoff, gbase, voff) do { _Pragma("unroll") for (int _i = 0; _i < 2; ++_i) \
;         __builtin_amdgcn_global_load_lds((const unsigned*)((const char*)(gbase) + (voff)[_i]), (PG8_LAS unsigned*)(lds + (bufoff) + ldsw + _i * 8192), 16, 0, 0); } while (0)
; #define PG8_LDA(dst, b, h) do { _Pragma("unroll") for (int m = 0; m < 4; ++m) { const bf16x8 f0_ = *(const PG8_LAS bf16x8*)(lds + PG8_SA(b, h) + aoff + m * 2048), f1_ = *(const PG8_LAS bf16x8*)(lds + PG8_SA(b, h) + aoff + m * 2048 + 1024); dst[m].set(f0_, f1_); } } while (0)
; #define PG8_LDB(dst, b, h) do { _Pragma("unroll") for (int n = 0; n < 2; ++n) { const bf16x8 f0_ = *(const PG8_LAS bf16x8*)(lds + PG8_SB(b, h) + boff + n * 2048), f1_ = *(const PG8_LAS bf16x8*)(lds + PG8_SB(b, h) + boff + n * 2048 + 1024); dst[n].set(f0_, f1_); } } while (0)
; #define PG8_WAIT_V(n) asm volatile("s_waitcnt vmcnt(" #n ")" ::: "memory")
; #define PG8_WAIT_L(n) asm volatile("s_waitcnt lgkmcnt(" #n ")" ::: "memory")
; #define PG8_BAR __builtin_amdgcn_s_barrier()
; #define PG8_SCHED __builtin_amdgcn_sched_barrier(0)
; template <class Epi, class Sched, bool ALIGN_EPI = false, bool SP2 = false>
; __device__ __forceinline__ void gemm_phase(PG8_LAS unsigned char* lds, const Gemm g, const Sched& S, const Epi& E) {
;     ...
;             PG8_LDA(At, 0, 1); PG8_STAGE(PG8_SB(0, 0), b2, voffB); PG8_STAGE(PG8_SB(0, 1), b2 + hstepB, voffB); PG8_STAGE(PG8_SA(0, 0), a2, voffA);
;             PG8_WAIT_V(8); PG8_WAIT_L(0); PG8_BAR; PG8_MMA(1, 0, At, B0); PG8_MMA(1, 1, At, B1); PG8_BAR; PG8_SCHED;
;             PG8_LDB(B0, 1, 0); PG8_LDB(B1, 1, 1); PG8_SCHED; PG8_LDA(At, 1, 0); PG8_STAGE(PG8_SA(0, 1), a2 + hstep, voffA);
;             PG8_WAIT_V(8); PG8_WAIT_L(0); PG8_BAR; PG8_MMA(0, 0, At, B0); PG8_MMA(0, 1, At, B1); PG8_BAR; PG8_SCHED;
	s_setprio 1
	s_waitcnt lgkmcnt(0)
	v_mfma_f32_16x16x32_bf16 v[62:65], v[168:171], v[206:209], v[62:65]
	v_mfma_f32_16x16x32_bf16 v[58:61], v[182:185], v[206:209], v[58:61]
	v_mfma_f32_16x16x32_bf16 v[46:49], v[168:171], v[216:219], v[46:49]
	v_mfma_f32_16x16x32_bf16 v[42:45], v[182:185], v[216:219], v[42:45]
	v_mfma_f32_16x16x32_bf16 v[30:33], v[168:171], v[224:227], v[30:33]
	v_mfma_f32_16x16x32_bf16 v[26:29], v[182:185], v[224:227], v[26:29]
	v_mfma_f32_16x16x32_bf16 v[14:17], v[168:171], v[232:235], v[14:17]
	v_mfma_f32_16x16x32_bf16 v[10:13], v[182:185], v[232:235], v[10:13]
	v_mfma_f32_16x16x32_bf16 v[62:65], v[178:181], v[212:215], v[62:65]
	v_mfma_f32_16x16x32_bf16 v[58:61], v[186:189], v[212:215], v[58:61]
	v_mfma_f32_16x16x32_bf16 v[46:49], v[178:181], v[220:223], v[46:49]
	v_mfma_f32_16x16x32_bf16 v[42:45], v[186:189], v[220:223], v[42:45]
	v_mfma_f32_16x16x32_bf16 v[30:33], v[178:181], v[228:231], v[30:33]
	v_mfma_f32_16x16x32_bf16 v[26:29], v[186:189], v[228:231], v[26:29]
	v_mfma_f32_16x16x32_bf16 v[14:17], v[178:181], v[236:239], v[14:17]
	v_mfma_f32_16x16x32_bf16 v[10:13], v[186:189], v[236:239], v[10:13]
	v_mfma_f32_16x16x32_bf16 v[54:57], v[190:193], v[206:209], v[54:57]
	v_mfma_f32_16x16x32_bf16 v[50:53], v[198:201], v[206:209], v[50:53]
	v_mfma_f32_16x16x32_bf16 v[38:41], v[190:193], v[216:219], v[38:41]
	v_mfma_f32_16x16x32_bf16 v[34:37], v[198:201], v[216:219], v[34:37]
	v_mfma_f32_16x16x32_bf16 v[22:25], v[190:193], v[224:227], v[22:25]
	v_mfma_f32_16x16x32_bf16 v[18:21], v[198:201], v[224:227], v[18:21]
	v_mfma_f32_16x16x32_bf16 v[6:9], v[190:193], v[232:235], v[6:9]
	v_mfma_f32_16x16x32_bf16 v[2:5], v[198:201], v[232:235], v[2:5]
	v_mfma_f32_16x16x32_bf16 v[54:57], v[194:197], v[212:215], v[54:57]
	v_mfma_f32_16x16x32_bf16 v[50:53], v[202:205], v[212:215], v[50:53]
	v_mfma_f32_16x16x32_bf16 v[38:41], v[194:197], v[220:223], v[38:41]
	v_mfma_f32_16x16x32_bf16 v[34:37], v[202:205], v[220:223], v[34:37]
	v_mfma_f32_16x16x32_bf16 v[22:25], v[194:197], v[228:231], v[22:25]
	v_mfma_f32_16x16x32_bf16 v[18:21], v[202:205], v[228:231], v[18:21]
	v_mfma_f32_16x16x32_bf16 v[6:9], v[194:197], v[236:239], v[6:9]
	v_mfma_f32_16x16x32_bf16 v[2:5], v[202:205], v[236:239], v[2:5]
	s_setprio 0
	s_barrier
	s_add_i32 s33, 0, 0x18000
	s_add_i32 s76, 0, 0x1c000
	v_add_u32_e32 v186, s33, v173
	v_add_u32_e32 v202, s76, v173
	ds_read_b128 v[168:171], v186
	ds_read_b128 v[178:181], v186 offset:1024
	ds_read_b128 v[182:185], v186 offset:2048
	ds_read_b128 v[186:189], v186 offset:3072
	ds_read_b128 v[190:193], v202
	ds_read_b128 v[194:197], v202 offset:1024
	ds_read_b128 v[198:201], v202 offset:2048
	ds_read_b128 v[202:205], v202 offset:3072
	s_add_u32 s0, s42, s12
	s_addc_u32 s1, s43, s13
	s_mov_b32 m0, s49
	v_lshl_add_u64 v[252:253], s[0:1], 0, v[130:131]
	ds_read_b128 v[206:209], v176 offset:32768
	ds_read_b128 v[212:215], v176 offset:33792
	ds_read_b128 v[216:219], v176 offset:34816
	ds_read_b128 v[220:223], v176 offset:35840
	ds_read_b128 v[224:227], v176 offset:36864
	ds_read_b128 v[228:231], v176 offset:37888
	ds_read_b128 v[232:235], v176 offset:38912
	ds_read_b128 v[236:239], v176 offset:39936
	s_mov_b32 m0, s47
	s_nop 0
	global_load_lds_dwordx4 v[248:249], off
	s_mov_b32 m0, s48
	s_nop 0
	global_load_lds_dwordx4 v[250:251], off
	s_mov_b32 m0, s49
	s_nop 0
	global_load_lds_dwordx4 v[252:253], off
	v_lshl_add_u64 v[252:253], s[0:1], 0, v[134:135]
	s_mov_b32 m0, s50
	s_nop 0
	global_load_lds_dwordx4 v[252:253], off
	s_waitcnt vmcnt(8)
	s_waitcnt lgkmcnt(0)
	s_barrier
; #define PG8_STAGE(bufoff, gbase, voff) do { _Pragma("unroll") for (int _i = 0; _i < 2; ++_i) \
;         __builtin_amdgcn_global_load_lds((const unsigned*)((const char*)(gbase) + (voff)[_i]), (PG8_LAS unsigned*)(lds + (bufoff) + ldsw + _i * 8192), 16, 0, 0); } while (0)
; #define PG8_LDA(dst, b, h) do { _Pragma("unroll") for (int m = 0; m < 4; ++m) { const bf16x8 f0_ = *(const PG8_LAS bf16x8*)(lds + PG8_SA(b, h) + aoff + m * 2048), f1_ = *(const PG8_LAS bf16x8*)(lds + PG8_SA(b, h) + aoff + m * 2048 + 1024); dst[m].set(f0_, f1_); } } while (0)
; #define PG8_LDB(dst, b, h) do { _Pragma("unroll") for (int n = 0; n < 2; ++n) { const bf16x8 f0_ = *(const PG8_LAS bf16x8*)(lds + PG8_SB(b, h) + boff + n * 2048), f1_ = *(const PG8_LAS bf16x8*)(lds + PG8_SB(b, h) + boff + n * 2048 + 1024); dst[n].set(f0_, f1_); } } while (0)
; #define PG8_WAIT_V(n) asm volatile("s_waitcnt vmcnt(" #n ")" ::: "memory")
; #define PG8_WAIT_L(n) asm volatile("s_waitcnt lgkmcnt(" #n ")" ::: "memory")
; #define PG8_BAR __builtin_amdgcn_s_barrier()
; #define PG8_SCHED __builtin_amdgcn_sched_barrier(0)
; template <class Epi, class Sched, bool ALIGN_EPI = false, bool SP2 = false>
; __device__ __forceinline__ void gemm_phase(PG8_LAS unsigned char* lds, const Gemm g, const Sched& S, const Epi& E) {
;     ...
;             PG8_LDB(B0, 1, 0); PG8_LDB(B1, 1, 1); PG8_SCHED; PG8_LDA(At, 1, 0); PG8_STAGE(PG8_SA(0, 1), a2 + hstep, voffA);
;             PG8_WAIT_V(8); PG8_WAIT_L(0); PG8_BAR; PG8_MMA(0, 0, At, B0); PG8_MMA(0, 1, At, B1); PG8_BAR; PG8_SCHED;
;             PG8_LDA(At, 1, 1); PG8_STAGE(PG8_SB(1, 0), b3, voffB); PG8_STAGE(PG8_SB(1, 1), b3 + hstepB, voffB); PG8_STAGE(PG8_SA(1, 0), a3, voffA);
;             PG8_WAIT_V(8); PG8_WAIT_L(0); PG8_BAR; PG8_MMA(1, 0, At, B0); PG8_MMA(1, 1, At, B1); PG8_BAR; PG8_SCHED;
	s_setprio 1
	s_waitcnt lgkmcnt(0)
	v_mfma_f32_16x16x32_bf16 v[126:129], v[168:171], v[206:209], v[126:129]
	v_mfma_f32_16x16x32_bf16 v[122:125], v[182:185], v[206:209], v[122:125]
	v_mfma_f32_16x16x32_bf16 v[110:113], v[168:171], v[216:219], v[110:113]
	v_mfma_f32_16x16x32_bf16 v[106:109], v[182:185], v[216:219], v[106:109]
	v_mfma_f32_16x16x32_bf16 v[94:97], v[168:171], v[224:227], v[94:97]
	v_mfma_f32_16x16x32_bf16 v[90:93], v[182:185], v[224:227], v[90:93]
	v_mfma_f32_16x16x32_bf16 v[78:81], v[168:171], v[232:235], v[78:81]
	v_mfma_f32_16x16x32_bf16 v[74:77], v[182:185], v[232:235], v[74:77]
	v_mfma_f32_16x16x32_bf16 v[126:129], v[178:181], v[212:215], v[126:129]
	v_mfma_f32_16x16x32_bf16 v[122:125], v[186:189], v[212:215], v[122:125]
	v_mfma_f32_16x16x32_bf16 v[110:113], v[178:181], v[220:223], v[110:113]
	v_mfma_f32_16x16x32_bf16 v[106:109], v[186:189], v[220:223], v[106:109]
	v_mfma_f32_16x16x32_bf16 v[94:97], v[178:181], v[228:231], v[94:97]
	v_mfma_f32_16x16x32_bf16 v[90:93], v[186:189], v[228:231], v[90:93]
	v_mfma_f32_16x16x32_bf16 v[78:81], v[178:181], v[236:239], v[78:81]
	v_mfma_f32_16x16x32_bf16 v[74:77], v[186:189], v[236:239], v[74:77]
	v_mfma_f32_16x16x32_bf16 v[118:121], v[190:193], v[206:209], v[118:121]
	v_mfma_f32_16x16x32_bf16 v[114:117], v[198:201], v[206:209], v[114:117]
	v_mfma_f32_16x16x32_bf16 v[102:105], v[190:193], v[216:219], v[102:105]
	v_mfma_f32_16x16x32_bf16 v[98:101], v[198:201], v[216:219], v[98:101]
	v_mfma_f32_16x16x32_bf16 v[86:89], v[190:193], v[224:227], v[86:89]
	v_mfma_f32_16x16x32_bf16 v[82:85], v[198:201], v[224:227], v[82:85]
	v_mfma_f32_16x16x32_bf16 v[70:73], v[190:193], v[232:235], v[70:73]
	v_mfma_f32_16x16x32_bf16 v[66:69], v[198:201], v[232:235], v[66:69]
	v_mfma_f32_16x16x32_bf16 v[118:121], v[194:197], v[212:215], v[118:121]
	v_mfma_f32_16x16x32_bf16 v[114:117], v[202:205], v[212:215], v[114:117]
	v_mfma_f32_16x16x32_bf16 v[102:105], v[194:197], v[220:223], v[102:105]
	v_mfma_f32_16x16x32_bf16 v[98:101], v[202:205], v[220:223], v[98:101]
	v_mfma_f32_16x16x32_bf16 v[86:89], v[194:197], v[228:231], v[86:89]
	v_mfma_f32_16x16x32_bf16 v[82:85], v[202:205], v[228:231], v[82:85]
	v_mfma_f32_16x16x32_bf16 v[70:73], v[194:197], v[236:239], v[70:73]
	v_mfma_f32_16x16x32_bf16 v[66:69], v[202:205], v[236:239], v[66:69]
	s_setprio 0
	s_barrier
	s_add_i32 s0, s33, s46
	v_lshl_add_u64 v[240:241], v[240:241], 0, s[26:27]
	s_mov_b32 m0, s0
	ds_read_b128 v[206:209], v176 offset:49152
	ds_read_b128 v[212:215], v176 offset:50176
	ds_read_b128 v[216:219], v176 offset:51200
	ds_read_b128 v[220:223], v176 offset:52224
	ds_read_b128 v[224:227], v176 offset:53248
	ds_read_b128 v[228:231], v176 offset:54272
	ds_read_b128 v[232:235], v176 offset:55296
	ds_read_b128 v[236:239], v176 offset:56320
	global_load_lds_dwordx4 v[240:241], off
	v_lshl_add_u64 v[240:241], v[242:243], 0, s[26:27]
	s_add_i32 m0, s0, 0x2000
	s_add_i32 s0, s76, s46
	global_load_lds_dwordx4 v[240:241], off
	v_lshl_add_u64 v[240:241], v[244:245], 0, s[26:27]
	s_mov_b32 m0, s0
	s_nop 0
	global_load_lds_dwordx4 v[240:241], off
	v_lshl_add_u64 v[240:241], v[246:247], 0, s[26:27]
	s_add_i32 m0, s0, 0x2000
	s_nop 0
	global_load_lds_dwordx4 v[240:241], off
	v_lshl_add_u64 v[240:241], v[248:249], 0, s[26:27]
	s_mov_b32 m0, s52
	s_nop 0
	global_load_lds_dwordx4 v[240:241], off
	v_lshl_add_u64 v[240:241], v[250:251], 0, s[26:27]
	s_mov_b32 m0, s53
	s_nop 0
	global_load_lds_dwordx4 v[240:241], off
	s_waitcnt vmcnt(6)
	s_waitcnt lgkmcnt(0)
	s_barrier
	s_setprio 1
	s_waitcnt lgkmcnt(0)
	v_mfma_f32_16x16x32_bf16 v[62:65], v[168:171], v[206:209], v[62:65]
	v_mfma_f32_16x16x32_bf16 v[58:61], v[182:185], v[206:209], v[58:61]
	v_mfma_f32_16x16x32_bf16 v[46:49], v[168:171], v[216:219], v[46:49]
	v_mfma_f32_16x16x32_bf16 v[42:45], v[182:185], v[216:219], v[42:45]
	v_mfma_f32_16x16x32_bf16 v[30:33], v[168:171], v[224:227], v[30:33]
	v_mfma_f32_16x16x32_bf16 v[26:29], v[182:185], v[224:227], v[26:29]
	v_mfma_f32_16x16x32_bf16 v[14:17], v[168:171], v[232:235], v[14:17]
	v_mfma_f32_16x16x32_bf16 v[10:13], v[182:185], v[232:235], v[10:13]
	v_mfma_f32_16x16x32_bf16 v[62:65], v[178:181], v[212:215], v[62:65]
	v_mfma_f32_16x16x32_bf16 v[58:61], v[186:189], v[212:215], v[58:61]
	v_mfma_f32_16x16x32_bf16 v[46:49], v[178:181], v[220:223], v[46:49]
	v_mfma_f32_16x16x32_bf16 v[42:45], v[186:189], v[220:223], v[42:45]
	v_mfma_f32_16x16x32_bf16 v[30:33], v[178:181], v[228:231], v[30:33]
	v_mfma_f32_16x16x32_bf16 v[26:29], v[186:189], v[228:231], v[26:29]
	v_mfma_f32_16x16x32_bf16 v[14:17], v[178:181], v[236:239], v[14:17]
	v_mfma_f32_16x16x32_bf16 v[10:13], v[186:189], v[236:239], v[10:13]
	v_mfma_f32_16x16x32_bf16 v[54:57], v[190:193], v[206:209], v[54:57]
	v_mfma_f32_16x16x32_bf16 v[50:53], v[198:201], v[206:209], v[50:53]
	v_mfma_f32_16x16x32_bf16 v[38:41], v[190:193], v[216:219], v[38:41]
	v_mfma_f32_16x16x32_bf16 v[34:37], v[198:201], v[216:219], v[34:37]
	v_mfma_f32_16x16x32_bf16 v[22:25], v[190:193], v[224:227], v[22:25]
	v_mfma_f32_16x16x32_bf16 v[18:21], v[198:201], v[224:227], v[18:21]
	v_mfma_f32_16x16x32_bf16 v[6:9], v[190:193], v[232:235], v[6:9]
	v_mfma_f32_16x16x32_bf16 v[2:5], v[198:201], v[232:235], v[2:5]
	v_mfma_f32_16x16x32_bf16 v[54:57], v[194:197], v[212:215], v[54:57]
	v_mfma_f32_16x16x32_bf16 v[50:53], v[202:205], v[212:215], v[50:53]
	v_mfma_f32_16x16x32_bf16 v[38:41], v[194:197], v[220:223], v[38:41]
	v_mfma_f32_16x16x32_bf16 v[34:37], v[202:205], v[220:223], v[34:37]
	v_mfma_f32_16x16x32_bf16 v[22:25], v[194:197], v[228:231], v[22:25]
	v_mfma_f32_16x16x32_bf16 v[18:21], v[202:205], v[228:231], v[18:21]
	v_mfma_f32_16x16x32_bf16 v[6:9], v[194:197], v[236:239], v[6:9]
	v_mfma_f32_16x16x32_bf16 v[2:5], v[202:205], v[236:239], v[2:5]
	s_setprio 0
	s_barrier
	s_add_u32 s40, s40, 0x100
	s_addc_u32 s41, s41, 0
	s_cmp_ge_i32 s75, s54
	s_cbranch_scc0 .LBB0_982

; #define PG8_STAGE(bufoff, gbase, voff) do { _Pragma("unroll") for (int _i = 0; _i < 2; ++_i) \
;         __builtin_amdgcn_global_load_lds((const unsigned*)((const char*)(gbase) + (voff)[_i]), (PG8_LAS unsigned*)(lds + (bufoff) + ldsw + _i * 8192), 16, 0, 0); } while (0)
; #define PG8_LDA(dst, b, h) do { _Pragma("unroll") for (int m = 0; m < 4; ++m) { const bf16x8 f0_ = *(const PG8_LAS bf16x8*)(lds + PG8_SA(b, h) + aoff + m * 2048), f1_ = *(const PG8_LAS bf16x8*)(lds + PG8_SA(b, h) + aoff + m * 2048 + 1024); dst[m].set(f0_, f1_); } } while (0)
; #define PG8_LDB(dst, b, h) do { _Pragma("unroll") for (int n = 0; n < 2; ++n) { const bf16x8 f0_ = *(const PG8_LAS bf16x8*)(lds + PG8_SB(b, h) + boff + n * 2048), f1_ = *(const PG8_LAS bf16x8*)(lds + PG8_SB(b, h) + boff + n * 2048 + 1024); dst[n].set(f0_, f1_); } } while (0)
; #define PG8_WAIT_V(n) asm volatile("s_waitcnt vmcnt(" #n ")" ::: "memory")
; #define PG8_WAIT_L(n) asm volatile("s_waitcnt lgkmcnt(" #n ")" ::: "memory")
; #define PG8_BAR __builtin_amdgcn_s_barrier()
; #define PG8_SCHED __builtin_amdgcn_sched_barrier(0)
; template <class Epi, class Sched, bool ALIGN_EPI = false, bool SP2 = false>
; __device__ __forceinline__ void gemm_phase(PG8_LAS unsigned char* lds, const Gemm g, const Sched& S, const Epi& E) {
;     ...
;             PG8_LDB(B0, 0, 0); PG8_LDB(B1, 0, 1); PG8_SCHED; PG8_LDA(At, 0, 0); PG8_STAGE(PG8_SA(1, 1), a1 + hstep, voffA);
;             PG8_WAIT_V(8); PG8_WAIT_L(0); PG8_BAR; PG8_MMA(0, 0, At, B0); PG8_MMA(0, 1, At, B1); PG8_BAR; PG8_SCHED;
;             PG8_LDA(At, 0, 1); PG8_STAGE(PG8_SB(0, 0), b2, voffB); PG8_STAGE(PG8_SB(0, 1), b2 + hstepB, voffB); PG8_STAGE(PG8_SA(0, 0), a2, voffA);
;             PG8_WAIT_V(8); PG8_WAIT_L(0); PG8_BAR; PG8_MMA(1, 0, At, B0); PG8_MMA(1, 1, At, B1); PG8_BAR; PG8_SCHED;
.Lkr2_a:
	v_lshl_add_u64 v[224:225], s[56:57], 0, v[176:177]
	s_add_i32 m0, s67, 0xc000
	ds_read_b128 v[162:165], v195
	ds_read_b128 v[186:189], v195 offset:1024
	ds_read_b128 v[198:201], v195 offset:2048
	ds_read_b128 v[202:205], v195 offset:3072
	ds_read_b128 v[206:209], v195 offset:4096
	ds_read_b128 v[212:215], v195 offset:5120
	ds_read_b128 v[216:219], v195 offset:6144
	ds_read_b128 v[220:223], v195 offset:7168
	global_load_lds_dwordx4 v[224:225], off
	v_lshl_add_u64 v[224:225], s[56:57], 0, v[178:179]
	s_add_i32 m0, s67, 0xe000
	s_nop 0
	global_load_lds_dwordx4 v[224:225], off
	s_waitcnt vmcnt(8)
	s_waitcnt lgkmcnt(0)
	s_barrier
	s_setprio 1
	s_waitcnt lgkmcnt(0)
	v_mfma_f32_16x16x32_bf16 v[126:129], v[130:133], v[162:165], v[126:129]
	v_mfma_f32_16x16x32_bf16 v[122:125], v[138:141], v[162:165], v[122:125]
	v_mfma_f32_16x16x32_bf16 v[58:61], v[130:133], v[198:201], v[58:61]
	v_mfma_f32_16x16x32_bf16 v[62:65], v[138:141], v[198:201], v[62:65]
	v_mfma_f32_16x16x32_bf16 v[106:109], v[130:133], v[206:209], v[106:109]
	v_mfma_f32_16x16x32_bf16 v[110:113], v[138:141], v[206:209], v[110:113]
	v_mfma_f32_16x16x32_bf16 v[98:101], v[130:133], v[216:219], v[98:101]
	v_mfma_f32_16x16x32_bf16 v[102:105], v[138:141], v[216:219], v[102:105]
	v_mfma_f32_16x16x32_bf16 v[126:129], v[134:137], v[186:189], v[126:129]
	v_mfma_f32_16x16x32_bf16 v[122:125], v[142:145], v[186:189], v[122:125]
	v_mfma_f32_16x16x32_bf16 v[58:61], v[134:137], v[202:205], v[58:61]
	v_mfma_f32_16x16x32_bf16 v[62:65], v[142:145], v[202:205], v[62:65]
	v_mfma_f32_16x16x32_bf16 v[106:109], v[134:137], v[212:215], v[106:109]
	v_mfma_f32_16x16x32_bf16 v[110:113], v[142:145], v[212:215], v[110:113]
	v_mfma_f32_16x16x32_bf16 v[98:101], v[134:137], v[220:223], v[98:101]
	v_mfma_f32_16x16x32_bf16 v[102:105], v[142:145], v[220:223], v[102:105]
	v_mfma_f32_16x16x32_bf16 v[118:121], v[146:149], v[162:165], v[118:121]
	v_mfma_f32_16x16x32_bf16 v[114:117], v[154:157], v[162:165], v[114:117]
	v_mfma_f32_16x16x32_bf16 v[50:53], v[146:149], v[198:201], v[50:53]
	v_mfma_f32_16x16x32_bf16 v[54:57], v[154:157], v[198:201], v[54:57]
	v_mfma_f32_16x16x32_bf16 v[90:93], v[146:149], v[206:209], v[90:93]
	v_mfma_f32_16x16x32_bf16 v[94:97], v[154:157], v[206:209], v[94:97]
	v_mfma_f32_16x16x32_bf16 v[74:77], v[146:149], v[216:219], v[74:77]
	v_mfma_f32_16x16x32_bf16 v[78:81], v[154:157], v[216:219], v[78:81]
	v_mfma_f32_16x16x32_bf16 v[118:121], v[150:153], v[186:189], v[118:121]
	v_mfma_f32_16x16x32_bf16 v[114:117], v[158:161], v[186:189], v[114:117]
	v_mfma_f32_16x16x32_bf16 v[50:53], v[150:153], v[202:205], v[50:53]
	v_mfma_f32_16x16x32_bf16 v[54:57], v[158:161], v[202:205], v[54:57]
	v_mfma_f32_16x16x32_bf16 v[90:93], v[150:153], v[212:215], v[90:93]
	v_mfma_f32_16x16x32_bf16 v[94:97], v[158:161], v[212:215], v[94:97]
	v_mfma_f32_16x16x32_bf16 v[74:77], v[150:153], v[220:223], v[74:77]
	v_mfma_f32_16x16x32_bf16 v[78:81], v[158:161], v[220:223], v[78:81]
	s_setprio 0
	s_barrier
	s_add_i32 s33, s82, s66
	v_lshl_add_u64 v[224:225], s[0:1], 0, v[168:169]
	s_mov_b32 m0, s33
	ds_read_b128 v[162:165], v195 offset:16384
	ds_read_b128 v[186:189], v195 offset:17408
	ds_read_b128 v[198:201], v195 offset:18432
	ds_read_b128 v[202:205], v195 offset:19456
	ds_read_b128 v[206:209], v195 offset:20480
	ds_read_b128 v[212:215], v195 offset:21504
	ds_read_b128 v[216:219], v195 offset:22528
	ds_read_b128 v[220:223], v195 offset:23552
	global_load_lds_dwordx4 v[224:225], off
	s_add_i32 m0, s33, 0x2000
	v_lshl_add_u64 v[226:227], s[0:1], 0, v[172:173]
	s_add_u32 s0, s0, s16
	s_addc_u32 s1, s1, s17
	s_add_i32 s33, s83, s66
	global_load_lds_dwordx4 v[226:227], off
	v_lshl_add_u64 v[228:229], s[0:1], 0, v[168:169]
	s_mov_b32 m0, s33
	v_lshl_add_u64 v[230:231], s[0:1], 0, v[172:173]
	global_load_lds_dwordx4 v[228:229], off
	s_add_i32 m0, s33, 0x2000
	v_lshl_add_u64 v[232:233], s[58:59], 0, v[166:167]
	global_load_lds_dwordx4 v[230:231], off
	v_lshl_add_u64 v[234:235], s[58:59], 0, v[170:171]
	s_waitcnt vmcnt(6)
	s_waitcnt lgkmcnt(0)
	s_barrier
	s_setprio 1
	s_waitcnt lgkmcnt(0)
	v_mfma_f32_16x16x32_bf16 v[82:85], v[130:133], v[162:165], v[82:85]
	v_mfma_f32_16x16x32_bf16 v[86:89], v[138:141], v[162:165], v[86:89]
	v_mfma_f32_16x16x32_bf16 v[46:49], v[130:133], v[198:201], v[46:49]
	v_mfma_f32_16x16x32_bf16 v[42:45], v[138:141], v[198:201], v[42:45]
	v_mfma_f32_16x16x32_bf16 v[30:33], v[130:133], v[206:209], v[30:33]
	v_mfma_f32_16x16x32_bf16 v[26:29], v[138:141], v[206:209], v[26:29]
	v_mfma_f32_16x16x32_bf16 v[14:17], v[130:133], v[216:219], v[14:17]
	v_mfma_f32_16x16x32_bf16 v[6:9], v[138:141], v[216:219], v[6:9]
	v_mfma_f32_16x16x32_bf16 v[82:85], v[134:137], v[186:189], v[82:85]
	v_mfma_f32_16x16x32_bf16 v[86:89], v[142:145], v[186:189], v[86:89]
	v_mfma_f32_16x16x32_bf16 v[46:49], v[134:137], v[202:205], v[46:49]
	v_mfma_f32_16x16x32_bf16 v[42:45], v[142:145], v[202:205], v[42:45]
	v_mfma_f32_16x16x32_bf16 v[30:33], v[134:137], v[212:215], v[30:33]
	v_mfma_f32_16x16x32_bf16 v[26:29], v[142:145], v[212:215], v[26:29]
	v_mfma_f32_16x16x32_bf16 v[14:17], v[134:137], v[220:223], v[14:17]
	v_mfma_f32_16x16x32_bf16 v[6:9], v[142:145], v[220:223], v[6:9]
	v_mfma_f32_16x16x32_bf16 v[66:69], v[146:149], v[162:165], v[66:69]
	v_mfma_f32_16x16x32_bf16 v[70:73], v[154:157], v[162:165], v[70:73]
	v_mfma_f32_16x16x32_bf16 v[38:41], v[146:149], v[198:201], v[38:41]
	v_mfma_f32_16x16x32_bf16 v[34:37], v[154:157], v[198:201], v[34:37]
	v_mfma_f32_16x16x32_bf16 v[22:25], v[146:149], v[206:209], v[22:25]
	v_mfma_f32_16x16x32_bf16 v[18:21], v[154:157], v[206:209], v[18:21]
	v_mfma_f32_16x16x32_bf16 v[10:13], v[146:149], v[216:219], v[10:13]
	v_mfma_f32_16x16x32_bf16 v[2:5], v[154:157], v[216:219], v[2:5]
	v_mfma_f32_16x16x32_bf16 v[66:69], v[150:153], v[186:189], v[66:69]
	v_mfma_f32_16x16x32_bf16 v[70:73], v[158:161], v[186:189], v[70:73]
	v_mfma_f32_16x16x32_bf16 v[38:41], v[150:153], v[202:205], v[38:41]
	v_mfma_f32_16x16x32_bf16 v[34:37], v[158:161], v[202:205], v[34:37]
	v_mfma_f32_16x16x32_bf16 v[22:25], v[150:153], v[212:215], v[22:25]
	v_mfma_f32_16x16x32_bf16 v[18:21], v[158:161], v[212:215], v[18:21]
	v_mfma_f32_16x16x32_bf16 v[10:13], v[150:153], v[220:223], v[10:13]
	v_mfma_f32_16x16x32_bf16 v[2:5], v[158:161], v[220:223], v[2:5]
	s_setprio 0
	s_barrier
; #define PG8_STAGE(bufoff, gbase, voff) do { _Pragma("unroll") for (int _i = 0; _i < 2; ++_i) \
;         __builtin_amdgcn_global_load_lds((const unsigned*)((const char*)(gbase) + (voff)[_i]), (PG8_LAS unsigned*)(lds + (bufoff) + ldsw + _i * 8192), 16, 0, 0); } while (0)
; #define PG8_LDA(dst, b, h) do { _Pragma("unroll") for (int m = 0; m < 4; ++m) { const bf16x8 f0_ = *(const PG8_LAS bf16x8*)(lds + PG8_SA(b, h) + aoff + m * 2048), f1_ = *(const PG8_LAS bf16x8*)(lds + PG8_SA(b, h) + aoff + m * 2048 + 1024); dst[m].set(f0_, f1_); } } while (0)
; #define PG8_LDB(dst, b, h) do { _Pragma("unroll") for (int n = 0; n < 2; ++n) { const bf16x8 f0_ = *(const PG8_LAS bf16x8*)(lds + PG8_SB(b, h) + boff + n * 2048), f1_ = *(const PG8_LAS bf16x8*)(lds + PG8_SB(b, h) + boff + n * 2048 + 1024); dst[n].set(f0_, f1_); } } while (0)
; #define PG8_WAIT_V(n) asm volatile("s_waitcnt vmcnt(" #n ")" ::: "memory")
; #define PG8_WAIT_L(n) asm volatile("s_waitcnt lgkmcnt(" #n ")" ::: "memory")
; #define PG8_BAR __builtin_amdgcn_s_barrier()
; #define PG8_SCHED __builtin_amdgcn_sched_barrier(0)
; template <class Epi, class Sched, bool ALIGN_EPI = false, bool SP2 = false>
; __device__ __forceinline__ void gemm_phase(PG8_LAS unsigned char* lds, const Gemm g, const Sched& S, const Epi& E) {
;     ...
;             PG8_WAIT_V(8); PG8_WAIT_L(0); PG8_BAR; PG8_MMA(1, 0, At, B0); PG8_MMA(1, 1, At, B1); PG8_BAR; PG8_SCHED;
;             PG8_LDB(B0, 1, 0); PG8_LDB(B1, 1, 1); PG8_SCHED; PG8_LDA(At, 1, 0); PG8_STAGE(PG8_SA(0, 1), a2 + hstep, voffA);
;             PG8_WAIT_V(8); PG8_WAIT_L(0); PG8_BAR; PG8_MMA(0, 0, At, B0); PG8_MMA(0, 1, At, B1); PG8_BAR; PG8_SCHED;
;             PG8_LDA(At, 1, 1); PG8_STAGE(PG8_SB(1, 0), b3, voffB); PG8_STAGE(PG8_SB(1, 1), b3 + hstepB, voffB); PG8_STAGE(PG8_SA(1, 0), a3, voffA);
	s_add_i32 s33, 0, 0x18000
	s_add_i32 s96, 0, 0x1c000
	v_add_u32_e32 v142, s33, v190
	v_add_u32_e32 v158, s96, v190
	ds_read_b128 v[130:133], v142
	ds_read_b128 v[134:137], v142 offset:1024
	ds_read_b128 v[138:141], v142 offset:2048
	ds_read_b128 v[142:145], v142 offset:3072
	ds_read_b128 v[146:149], v158
	ds_read_b128 v[150:153], v158 offset:1024
	ds_read_b128 v[154:157], v158 offset:2048
	ds_read_b128 v[158:161], v158 offset:3072
	s_add_u32 s0, s58, s14
	s_addc_u32 s1, s59, s15
	s_mov_b32 m0, s71
	v_lshl_add_u64 v[236:237], s[0:1], 0, v[166:167]
	ds_read_b128 v[162:165], v195 offset:32768
	ds_read_b128 v[186:189], v195 offset:33792
	ds_read_b128 v[198:201], v195 offset:34816
	ds_read_b128 v[202:205], v195 offset:35840
	ds_read_b128 v[206:209], v195 offset:36864
	ds_read_b128 v[212:215], v195 offset:37888
	ds_read_b128 v[216:219], v195 offset:38912
	ds_read_b128 v[220:223], v195 offset:39936
	s_mov_b32 m0, s67
	s_nop 0
	global_load_lds_dwordx4 v[232:233], off
	s_mov_b32 m0, s69
	s_nop 0
	global_load_lds_dwordx4 v[234:235], off
	s_mov_b32 m0, s71
	s_nop 0
	global_load_lds_dwordx4 v[236:237], off
	v_lshl_add_u64 v[236:237], s[0:1], 0, v[170:171]
	s_mov_b32 m0, s73
	s_nop 0
	global_load_lds_dwordx4 v[236:237], off
	s_waitcnt vmcnt(8)
	s_waitcnt lgkmcnt(0)
	s_barrier
	s_setprio 1
	s_waitcnt lgkmcnt(0)
	v_mfma_f32_16x16x32_bf16 v[126:129], v[130:133], v[162:165], v[126:129]
	v_mfma_f32_16x16x32_bf16 v[122:125], v[138:141], v[162:165], v[122:125]
	v_mfma_f32_16x16x32_bf16 v[58:61], v[130:133], v[198:201], v[58:61]
	v_mfma_f32_16x16x32_bf16 v[62:65], v[138:141], v[198:201], v[62:65]
	v_mfma_f32_16x16x32_bf16 v[106:109], v[130:133], v[206:209], v[106:109]
	v_mfma_f32_16x16x32_bf16 v[110:113], v[138:141], v[206:209], v[110:113]
	v_mfma_f32_16x16x32_bf16 v[98:101], v[130:133], v[216:219], v[98:101]
	v_mfma_f32_16x16x32_bf16 v[102:105], v[138:141], v[216:219], v[102:105]
	v_mfma_f32_16x16x32_bf16 v[126:129], v[134:137], v[186:189], v[126:129]
	v_mfma_f32_16x16x32_bf16 v[122:125], v[142:145], v[186:189], v[122:125]
	v_mfma_f32_16x16x32_bf16 v[58:61], v[134:137], v[202:205], v[58:61]
	v_mfma_f32_16x16x32_bf16 v[62:65], v[142:145], v[202:205], v[62:65]
	v_mfma_f32_16x16x32_bf16 v[106:109], v[134:137], v[212:215], v[106:109]
	v_mfma_f32_16x16x32_bf16 v[110:113], v[142:145], v[212:215], v[110:113]
	v_mfma_f32_16x16x32_bf16 v[98:101], v[134:137], v[220:223], v[98:101]
	v_mfma_f32_16x16x32_bf16 v[102:105], v[142:145], v[220:223], v[102:105]
	v_mfma_f32_16x16x32_bf16 v[118:121], v[146:149], v[162:165], v[118:121]
	v_mfma_f32_16x16x32_bf16 v[114:117], v[154:157], v[162:165], v[114:117]
	v_mfma_f32_16x16x32_bf16 v[50:53], v[146:149], v[198:201], v[50:53]
	v_mfma_f32_16x16x32_bf16 v[54:57], v[154:157], v[198:201], v[54:57]
	v_mfma_f32_16x16x32_bf16 v[90:93], v[146:149], v[206:209], v[90:93]
	v_mfma_f32_16x16x32_bf16 v[94:97], v[154:157], v[206:209], v[94:97]
	v_mfma_f32_16x16x32_bf16 v[74:77], v[146:149], v[216:219], v[74:77]
	v_mfma_f32_16x16x32_bf16 v[78:81], v[154:157], v[216:219], v[78:81]
	v_mfma_f32_16x16x32_bf16 v[118:121], v[150:153], v[186:189], v[118:121]
	v_mfma_f32_16x16x32_bf16 v[114:117], v[158:161], v[186:189], v[114:117]
	v_mfma_f32_16x16x32_bf16 v[50:53], v[150:153], v[202:205], v[50:53]
	v_mfma_f32_16x16x32_bf16 v[54:57], v[158:161], v[202:205], v[54:57]
	v_mfma_f32_16x16x32_bf16 v[90:93], v[150:153], v[212:215], v[90:93]
	v_mfma_f32_16x16x32_bf16 v[94:97], v[158:161], v[212:215], v[94:97]
	v_mfma_f32_16x16x32_bf16 v[74:77], v[150:153], v[220:223], v[74:77]
	v_mfma_f32_16x16x32_bf16 v[78:81], v[158:161], v[220:223], v[78:81]
	s_setprio 0
	s_barrier
	s_add_i32 s0, s33, s66
	v_lshl_add_u64 v[224:225], v[224:225], 0, s[28:29]
	s_mov_b32 m0, s0
	ds_read_b128 v[162:165], v195 offset:49152
	ds_read_b128 v[186:189], v195 offset:50176
	ds_read_b128 v[198:201], v195 offset:51200
	ds_read_b128 v[202:205], v195 offset:52224
	ds_read_b128 v[206:209], v195 offset:53248
	ds_read_b128 v[212:215], v195 offset:54272
	ds_read_b128 v[216:219], v195 offset:55296
	ds_read_b128 v[220:223], v195 offset:56320
	global_load_lds_dwordx4 v[224:225], off
	v_lshl_add_u64 v[224:225], v[226:227], 0, s[28:29]
	s_add_i32 m0, s0, 0x2000
	s_add_i32 s0, s96, s66
	global_load_lds_dwordx4 v[224:225], off
	v_lshl_add_u64 v[224:225], v[228:229], 0, s[28:29]
	s_mov_b32 m0, s0
	s_nop 0
	global_load_lds_dwordx4 v[224:225], off
	v_lshl_add_u64 v[224:225], v[230:231], 0, s[28:29]
	s_add_i32 m0, s0, 0x2000
	s_nop 0
	global_load_lds_dwordx4 v[224:225], off
	s_cmp_ge_i32 s95, s76
	s_cbranch_scc0 .Lkr2_b
	v_lshl_add_u64 v[224:225], v[232:233], 0, s[28:29]
	s_mov_b32 m0, s74
	s_nop 0
	global_load_lds_dwordx4 v[224:225], off
	v_lshl_add_u64 v[224:225], v[234:235], 0, s[28:29]
	s_mov_b32 m0, s75
	s_nop 0
	global_load_lds_dwordx4 v[224:225], off
; #define PG8_STAGE(bufoff, gbase, voff) do { _Pragma("unroll") for (int _i = 0; _i < 2; ++_i) \
;         __builtin_amdgcn_global_load_lds((const unsigned*)((const char*)(gbase) + (voff)[_i]), (PG8_LAS unsigned*)(lds + (bufoff) + ldsw + _i * 8192), 16, 0, 0); } while (0)
; #define PG8_LDA(dst, b, h) do { _Pragma("unroll") for (int m = 0; m < 4; ++m) { const bf16x8 f0_ = *(const PG8_LAS bf16x8*)(lds + PG8_SA(b, h) + aoff + m * 2048), f1_ = *(const PG8_LAS bf16x8*)(lds + PG8_SA(b, h) + aoff + m * 2048 + 1024); dst[m].set(f0_, f1_); } } while (0)
; #define PG8_WAIT_V(n) asm volatile("s_waitcnt vmcnt(" #n ")" ::: "memory")
; #define PG8_WAIT_L(n) asm volatile("s_waitcnt lgkmcnt(" #n ")" ::: "memory")
; #define PG8_BAR __builtin_amdgcn_s_barrier()
; #define PG8_SCHED __builtin_amdgcn_sched_barrier(0)
; template <class Epi, class Sched, bool ALIGN_EPI = false, bool SP2 = false>
; __device__ __forceinline__ void gemm_phase(PG8_LAS unsigned char* lds, const Gemm g, const Sched& S, const Epi& E) {
;     ...
;         for (int t = 0; t < nt; t += 2) {
;             if constexpr (Epi::MIDK) { if (t == (nt >> 1)) E.mid(acc, cur, wr, wc, fr, fq); }
;             const bool last = (t == nt - 2);
;             const char* a1 = cA + (size_t)(t + 1) * kstep;
;             const char* a2 = last ? nA : cA + (size_t)(t + 2) * kstep; const char* b2 = last ? nB : cB + (size_t)(t + 2) * kstep;
;             const char* a3 = a2 + kstep; const char* b3 = b2 + kstep;
;     ...
;             PG8_LDA(At, 1, 1); PG8_STAGE(PG8_SB(1, 0), b3, voffB); PG8_STAGE(PG8_SB(1, 1), b3 + hstepB, voffB); PG8_STAGE(PG8_SA(1, 0), a3, voffA);
;             PG8_WAIT_V(8); PG8_WAIT_L(0); PG8_BAR; PG8_MMA(1, 0, At, B0); PG8_MMA(1, 1, At, B1); PG8_BAR; PG8_SCHED;
.Lkr2_b:
	s_waitcnt vmcnt(6)
	s_waitcnt lgkmcnt(0)
	s_barrier
	s_setprio 1
	s_waitcnt lgkmcnt(0)
	v_mfma_f32_16x16x32_bf16 v[82:85], v[130:133], v[162:165], v[82:85]
	v_mfma_f32_16x16x32_bf16 v[86:89], v[138:141], v[162:165], v[86:89]
	v_mfma_f32_16x16x32_bf16 v[46:49], v[130:133], v[198:201], v[46:49]
	v_mfma_f32_16x16x32_bf16 v[42:45], v[138:141], v[198:201], v[42:45]
	v_mfma_f32_16x16x32_bf16 v[30:33], v[130:133], v[206:209], v[30:33]
	v_mfma_f32_16x16x32_bf16 v[26:29], v[138:141], v[206:209], v[26:29]
	v_mfma_f32_16x16x32_bf16 v[14:17], v[130:133], v[216:219], v[14:17]
	v_mfma_f32_16x16x32_bf16 v[6:9], v[138:141], v[216:219], v[6:9]
	v_mfma_f32_16x16x32_bf16 v[82:85], v[134:137], v[186:189], v[82:85]
	v_mfma_f32_16x16x32_bf16 v[86:89], v[142:145], v[186:189], v[86:89]
	v_mfma_f32_16x16x32_bf16 v[46:49], v[134:137], v[202:205], v[46:49]
	v_mfma_f32_16x16x32_bf16 v[42:45], v[142:145], v[202:205], v[42:45]
	v_mfma_f32_16x16x32_bf16 v[30:33], v[134:137], v[212:215], v[30:33]
	v_mfma_f32_16x16x32_bf16 v[26:29], v[142:145], v[212:215], v[26:29]
	v_mfma_f32_16x16x32_bf16 v[14:17], v[134:137], v[220:223], v[14:17]
	v_mfma_f32_16x16x32_bf16 v[6:9], v[142:145], v[220:223], v[6:9]
	v_mfma_f32_16x16x32_bf16 v[66:69], v[146:149], v[162:165], v[66:69]
	v_mfma_f32_16x16x32_bf16 v[70:73], v[154:157], v[162:165], v[70:73]
	v_mfma_f32_16x16x32_bf16 v[38:41], v[146:149], v[198:201], v[38:41]
	v_mfma_f32_16x16x32_bf16 v[34:37], v[154:157], v[198:201], v[34:37]
	v_mfma_f32_16x16x32_bf16 v[22:25], v[146:149], v[206:209], v[22:25]
	v_mfma_f32_16x16x32_bf16 v[18:21], v[154:157], v[206:209], v[18:21]
	v_mfma_f32_16x16x32_bf16 v[10:13], v[146:149], v[216:219], v[10:13]
	v_mfma_f32_16x16x32_bf16 v[2:5], v[154:157], v[216:219], v[2:5]
	v_mfma_f32_16x16x32_bf16 v[66:69], v[150:153], v[186:189], v[66:69]
	v_mfma_f32_16x16x32_bf16 v[70:73], v[158:161], v[186:189], v[70:73]
	v_mfma_f32_16x16x32_bf16 v[38:41], v[150:153], v[202:205], v[38:41]
	v_mfma_f32_16x16x32_bf16 v[34:37], v[158:161], v[202:205], v[34:37]
	v_mfma_f32_16x16x32_bf16 v[22:25], v[150:153], v[212:215], v[22:25]
	v_mfma_f32_16x16x32_bf16 v[18:21], v[158:161], v[212:215], v[18:21]
	v_mfma_f32_16x16x32_bf16 v[10:13], v[150:153], v[220:223], v[10:13]
	v_mfma_f32_16x16x32_bf16 v[2:5], v[158:161], v[220:223], v[2:5]
	s_setprio 0
	s_barrier
	s_add_u32 s56, s56, 0x100
	s_addc_u32 s57, s57, 0
	s_add_u32 s93, s93, 0x100
	s_addc_u32 s94, s94, 0
	s_cmp_ge_i32 s95, s76
	s_cselect_b32 s99, 0, 1
	s_mov_b32 s58, s95
	s_cbranch_scc0 .LBB0_1070
	v_readlane_b32 s94, v254, 5
	v_readlane_b32 s95, v254, 6

; #define PG8_STAGE(bufoff, gbase, voff) do { _Pragma("unroll") for (int _i = 0; _i < 2; ++_i) \
;         __builtin_amdgcn_global_load_lds((const unsigned*)((const char*)(gbase) + (voff)[_i]), (PG8_LAS unsigned*)(lds + (bufoff) + ldsw + _i * 8192), 16, 0, 0); } while (0)
; #define PG8_LDA(dst, b, h) do { _Pragma("unroll") for (int m = 0; m < 4; ++m) { const bf16x8 f0_ = *(const PG8_LAS bf16x8*)(lds + PG8_SA(b, h) + aoff + m * 2048), f1_ = *(const PG8_LAS bf16x8*)(lds + PG8_SA(b, h) + aoff + m * 2048 + 1024); dst[m].set(f0_, f1_); } } while (0)
; #define PG8_LDB(dst, b, h) do { _Pragma("unroll") for (int n = 0; n < 2; ++n) { const bf16x8 f0_ = *(const PG8_LAS bf16x8*)(lds + PG8_SB(b, h) + boff + n * 2048), f1_ = *(const PG8_LAS bf16x8*)(lds + PG8_SB(b, h) + boff + n * 2048 + 1024); dst[n].set(f0_, f1_); } } while (0)
; #define PG8_WAIT_V(n) asm volatile("s_waitcnt vmcnt(" #n ")" ::: "memory")
; #define PG8_WAIT_L(n) asm volatile("s_waitcnt lgkmcnt(" #n ")" ::: "memory")
; #define PG8_BAR __builtin_amdgcn_s_barrier()
; #define PG8_SCHED __builtin_amdgcn_sched_barrier(0)
; template <class Epi, class Sched, bool ALIGN_EPI = false, bool SP2 = false>
; __device__ __forceinline__ void gemm_phase(PG8_LAS unsigned char* lds, const Gemm g, const Sched& S, const Epi& E) {
;     ...
;             PG8_LDB(B0, 0, 0); PG8_LDB(B1, 0, 1); PG8_SCHED; PG8_LDA(At, 0, 0); PG8_STAGE(PG8_SA(1, 1), a1 + hstep, voffA);
;             PG8_WAIT_V(8); PG8_WAIT_L(0); PG8_BAR; PG8_MMA(0, 0, At, B0); PG8_MMA(0, 1, At, B1); PG8_BAR; PG8_SCHED;
;             PG8_LDA(At, 0, 1); PG8_STAGE(PG8_SB(0, 0), b2, voffB); PG8_STAGE(PG8_SB(0, 1), b2 + hstepB, voffB); PG8_STAGE(PG8_SA(0, 0), a2, voffA);
;             PG8_WAIT_V(8); PG8_WAIT_L(0); PG8_BAR; PG8_MMA(1, 0, At, B0); PG8_MMA(1, 1, At, B1); PG8_BAR; PG8_SCHED;
.Lkr3_a:
	v_lshl_add_u64 v[148:149], s[30:31], 0, v[140:141]
	s_add_i32 m0, s40, 0xc000
	ds_read_b128 v[188:191], v154
	ds_read_b128 v[192:195], v154 offset:1024
	ds_read_b128 v[196:199], v154 offset:2048
	ds_read_b128 v[200:203], v154 offset:3072
	ds_read_b128 v[204:207], v154 offset:4096
	ds_read_b128 v[212:215], v154 offset:5120
	ds_read_b128 v[216:219], v154 offset:6144
	ds_read_b128 v[220:223], v154 offset:7168
	global_load_lds_dwordx4 v[148:149], off
	v_lshl_add_u64 v[148:149], s[30:31], 0, v[142:143]
	s_add_i32 m0, s40, 0xe000
	s_nop 0
	global_load_lds_dwordx4 v[148:149], off
	s_waitcnt vmcnt(8)
	s_waitcnt lgkmcnt(0)
	s_barrier
	s_setprio 1
	s_waitcnt lgkmcnt(0)
	v_mfma_f32_16x16x32_bf16 v[126:129], v[156:159], v[188:191], v[126:129]
	v_mfma_f32_16x16x32_bf16 v[122:125], v[164:167], v[188:191], v[122:125]
	v_mfma_f32_16x16x32_bf16 v[110:113], v[156:159], v[196:199], v[110:113]
	v_mfma_f32_16x16x32_bf16 v[106:109], v[164:167], v[196:199], v[106:109]
	v_mfma_f32_16x16x32_bf16 v[94:97], v[156:159], v[204:207], v[94:97]
	v_mfma_f32_16x16x32_bf16 v[90:93], v[164:167], v[204:207], v[90:93]
	v_mfma_f32_16x16x32_bf16 v[78:81], v[156:159], v[216:219], v[78:81]
	v_mfma_f32_16x16x32_bf16 v[74:77], v[164:167], v[216:219], v[74:77]
	v_mfma_f32_16x16x32_bf16 v[126:129], v[160:163], v[192:195], v[126:129]
	v_mfma_f32_16x16x32_bf16 v[122:125], v[168:171], v[192:195], v[122:125]
	v_mfma_f32_16x16x32_bf16 v[110:113], v[160:163], v[200:203], v[110:113]
	v_mfma_f32_16x16x32_bf16 v[106:109], v[168:171], v[200:203], v[106:109]
	v_mfma_f32_16x16x32_bf16 v[94:97], v[160:163], v[212:215], v[94:97]
	v_mfma_f32_16x16x32_bf16 v[90:93], v[168:171], v[212:215], v[90:93]
	v_mfma_f32_16x16x32_bf16 v[78:81], v[160:163], v[220:223], v[78:81]
	v_mfma_f32_16x16x32_bf16 v[74:77], v[168:171], v[220:223], v[74:77]
	v_mfma_f32_16x16x32_bf16 v[118:121], v[172:175], v[188:191], v[118:121]
	v_mfma_f32_16x16x32_bf16 v[114:117], v[180:183], v[188:191], v[114:117]
	v_mfma_f32_16x16x32_bf16 v[102:105], v[172:175], v[196:199], v[102:105]
	v_mfma_f32_16x16x32_bf16 v[98:101], v[180:183], v[196:199], v[98:101]
	v_mfma_f32_16x16x32_bf16 v[86:89], v[172:175], v[204:207], v[86:89]
	v_mfma_f32_16x16x32_bf16 v[82:85], v[180:183], v[204:207], v[82:85]
	v_mfma_f32_16x16x32_bf16 v[70:73], v[172:175], v[216:219], v[70:73]
	v_mfma_f32_16x16x32_bf16 v[66:69], v[180:183], v[216:219], v[66:69]
	v_mfma_f32_16x16x32_bf16 v[118:121], v[176:179], v[192:195], v[118:121]
	v_mfma_f32_16x16x32_bf16 v[114:117], v[184:187], v[192:195], v[114:117]
	v_mfma_f32_16x16x32_bf16 v[102:105], v[176:179], v[200:203], v[102:105]
	v_mfma_f32_16x16x32_bf16 v[98:101], v[184:187], v[200:203], v[98:101]
	v_mfma_f32_16x16x32_bf16 v[86:89], v[176:179], v[212:215], v[86:89]
	v_mfma_f32_16x16x32_bf16 v[82:85], v[184:187], v[212:215], v[82:85]
	v_mfma_f32_16x16x32_bf16 v[70:73], v[176:179], v[220:223], v[70:73]
	v_mfma_f32_16x16x32_bf16 v[66:69], v[184:187], v[220:223], v[66:69]
	s_setprio 0
	s_barrier
	s_add_i32 s33, s52, s39
	v_lshl_add_u64 v[148:149], s[0:1], 0, v[132:133]
	s_mov_b32 m0, s33
	ds_read_b128 v[188:191], v154 offset:16384
	ds_read_b128 v[192:195], v154 offset:17408
	ds_read_b128 v[196:199], v154 offset:18432
	ds_read_b128 v[200:203], v154 offset:19456
	ds_read_b128 v[204:207], v154 offset:20480
	ds_read_b128 v[212:215], v154 offset:21504
	ds_read_b128 v[216:219], v154 offset:22528
	ds_read_b128 v[220:223], v154 offset:23552
	global_load_lds_dwordx4 v[148:149], off
	s_add_i32 m0, s33, 0x2000
	v_lshl_add_u64 v[208:209], s[0:1], 0, v[136:137]
	s_add_u32 s0, s0, s14
	s_addc_u32 s1, s1, s15
	s_add_i32 s33, s53, s39
	global_load_lds_dwordx4 v[208:209], off
	v_lshl_add_u64 v[224:225], s[0:1], 0, v[132:133]
	s_mov_b32 m0, s33
	v_lshl_add_u64 v[226:227], s[0:1], 0, v[136:137]
	global_load_lds_dwordx4 v[224:225], off
	s_add_i32 m0, s33, 0x2000
	v_lshl_add_u64 v[228:229], s[34:35], 0, v[130:131]
	global_load_lds_dwordx4 v[226:227], off
	v_lshl_add_u64 v[230:231], s[34:35], 0, v[134:135]
	s_waitcnt vmcnt(6)
	s_waitcnt lgkmcnt(0)
	s_barrier
	s_setprio 1
	s_waitcnt lgkmcnt(0)
	v_mfma_f32_16x16x32_bf16 v[62:65], v[156:159], v[188:191], v[62:65]
	v_mfma_f32_16x16x32_bf16 v[58:61], v[164:167], v[188:191], v[58:61]
	v_mfma_f32_16x16x32_bf16 v[46:49], v[156:159], v[196:199], v[46:49]
	v_mfma_f32_16x16x32_bf16 v[42:45], v[164:167], v[196:199], v[42:45]
	v_mfma_f32_16x16x32_bf16 v[30:33], v[156:159], v[204:207], v[30:33]
	v_mfma_f32_16x16x32_bf16 v[26:29], v[164:167], v[204:207], v[26:29]
	v_mfma_f32_16x16x32_bf16 v[14:17], v[156:159], v[216:219], v[14:17]
	v_mfma_f32_16x16x32_bf16 v[6:9], v[164:167], v[216:219], v[6:9]
	v_mfma_f32_16x16x32_bf16 v[62:65], v[160:163], v[192:195], v[62:65]
	v_mfma_f32_16x16x32_bf16 v[58:61], v[168:171], v[192:195], v[58:61]
	v_mfma_f32_16x16x32_bf16 v[46:49], v[160:163], v[200:203], v[46:49]
	v_mfma_f32_16x16x32_bf16 v[42:45], v[168:171], v[200:203], v[42:45]
	v_mfma_f32_16x16x32_bf16 v[30:33], v[160:163], v[212:215], v[30:33]
	v_mfma_f32_16x16x32_bf16 v[26:29], v[168:171], v[212:215], v[26:29]
	v_mfma_f32_16x16x32_bf16 v[14:17], v[160:163], v[220:223], v[14:17]
	v_mfma_f32_16x16x32_bf16 v[6:9], v[168:171], v[220:223], v[6:9]
	v_mfma_f32_16x16x32_bf16 v[54:57], v[172:175], v[188:191], v[54:57]
	v_mfma_f32_16x16x32_bf16 v[50:53], v[180:183], v[188:191], v[50:53]
	v_mfma_f32_16x16x32_bf16 v[38:41], v[172:175], v[196:199], v[38:41]
	v_mfma_f32_16x16x32_bf16 v[34:37], v[180:183], v[196:199], v[34:37]
	v_mfma_f32_16x16x32_bf16 v[22:25], v[172:175], v[204:207], v[22:25]
	v_mfma_f32_16x16x32_bf16 v[18:21], v[180:183], v[204:207], v[18:21]
	v_mfma_f32_16x16x32_bf16 v[10:13], v[172:175], v[216:219], v[10:13]
	v_mfma_f32_16x16x32_bf16 v[2:5], v[180:183], v[216:219], v[2:5]
	v_mfma_f32_16x16x32_bf16 v[54:57], v[176:179], v[192:195], v[54:57]
	v_mfma_f32_16x16x32_bf16 v[50:53], v[184:187], v[192:195], v[50:53]
	v_mfma_f32_16x16x32_bf16 v[38:41], v[176:179], v[200:203], v[38:41]
	v_mfma_f32_16x16x32_bf16 v[34:37], v[184:187], v[200:203], v[34:37]
	v_mfma_f32_16x16x32_bf16 v[22:25], v[176:179], v[212:215], v[22:25]
	v_mfma_f32_16x16x32_bf16 v[18:21], v[184:187], v[212:215], v[18:21]
	v_mfma_f32_16x16x32_bf16 v[10:13], v[176:179], v[220:223], v[10:13]
	v_mfma_f32_16x16x32_bf16 v[2:5], v[184:187], v[220:223], v[2:5]
	s_setprio 0
	s_barrier
; #define PG8_STAGE(bufoff, gbase, voff) do { _Pragma("unroll") for (int _i = 0; _i < 2; ++_i) \
;         __builtin_amdgcn_global_load_lds((const unsigned*)((const char*)(gbase) + (voff)[_i]), (PG8_LAS unsigned*)(lds + (bufoff) + ldsw + _i * 8192), 16, 0, 0); } while (0)
; #define PG8_LDA(dst, b, h) do { _Pragma("unroll") for (int m = 0; m < 4; ++m) { const bf16x8 f0_ = *(const PG8_LAS bf16x8*)(lds + PG8_SA(b, h) + aoff + m * 2048), f1_ = *(const PG8_LAS bf16x8*)(lds + PG8_SA(b, h) + aoff + m * 2048 + 1024); dst[m].set(f0_, f1_); } } while (0)
; #define PG8_LDB(dst, b, h) do { _Pragma("unroll") for (int n = 0; n < 2; ++n) { const bf16x8 f0_ = *(const PG8_LAS bf16x8*)(lds + PG8_SB(b, h) + boff + n * 2048), f1_ = *(const PG8_LAS bf16x8*)(lds + PG8_SB(b, h) + boff + n * 2048 + 1024); dst[n].set(f0_, f1_); } } while (0)
; #define PG8_WAIT_V(n) asm volatile("s_waitcnt vmcnt(" #n ")" ::: "memory")
; #define PG8_WAIT_L(n) asm volatile("s_waitcnt lgkmcnt(" #n ")" ::: "memory")
; #define PG8_BAR __builtin_amdgcn_s_barrier()
; #define PG8_SCHED __builtin_amdgcn_sched_barrier(0)
; template <class Epi, class Sched, bool ALIGN_EPI = false, bool SP2 = false>
; __device__ __forceinline__ void gemm_phase(PG8_LAS unsigned char* lds, const Gemm g, const Sched& S, const Epi& E) {
;     ...
;             PG8_WAIT_V(8); PG8_WAIT_L(0); PG8_BAR; PG8_MMA(1, 0, At, B0); PG8_MMA(1, 1, At, B1); PG8_BAR; PG8_SCHED;
;             PG8_LDB(B0, 1, 0); PG8_LDB(B1, 1, 1); PG8_SCHED; PG8_LDA(At, 1, 0); PG8_STAGE(PG8_SA(0, 1), a2 + hstep, voffA);
;             PG8_WAIT_V(8); PG8_WAIT_L(0); PG8_BAR; PG8_MMA(0, 0, At, B0); PG8_MMA(0, 1, At, B1); PG8_BAR; PG8_SCHED;
;             PG8_LDA(At, 1, 1); PG8_STAGE(PG8_SB(1, 0), b3, voffB); PG8_STAGE(PG8_SB(1, 1), b3 + hstepB, voffB); PG8_STAGE(PG8_SA(1, 0), a3, voffA);
	s_add_i32 s33, 0, 0x18000
	s_add_i32 s63, 0, 0x1c000
	v_add_u32_e32 v168, s33, v1
	v_add_u32_e32 v184, s63, v1
	ds_read_b128 v[156:159], v168
	ds_read_b128 v[160:163], v168 offset:1024
	ds_read_b128 v[164:167], v168 offset:2048
	ds_read_b128 v[168:171], v168 offset:3072
	ds_read_b128 v[172:175], v184
	ds_read_b128 v[176:179], v184 offset:1024
	ds_read_b128 v[180:183], v184 offset:2048
	ds_read_b128 v[184:187], v184 offset:3072
	s_add_u32 s0, s34, s12
	s_addc_u32 s1, s35, s13
	s_mov_b32 m0, s42
	v_lshl_add_u64 v[232:233], s[0:1], 0, v[130:131]
	ds_read_b128 v[188:191], v154 offset:32768
	ds_read_b128 v[192:195], v154 offset:33792
	ds_read_b128 v[196:199], v154 offset:34816
	ds_read_b128 v[200:203], v154 offset:35840
	ds_read_b128 v[204:207], v154 offset:36864
	ds_read_b128 v[212:215], v154 offset:37888
	ds_read_b128 v[216:219], v154 offset:38912
	ds_read_b128 v[220:223], v154 offset:39936
	s_mov_b32 m0, s40
	s_nop 0
	global_load_lds_dwordx4 v[228:229], off
	s_mov_b32 m0, s41
	s_nop 0
	global_load_lds_dwordx4 v[230:231], off
	s_mov_b32 m0, s42
	s_nop 0
	global_load_lds_dwordx4 v[232:233], off
	v_lshl_add_u64 v[232:233], s[0:1], 0, v[134:135]
	s_mov_b32 m0, s43
	s_nop 0
	global_load_lds_dwordx4 v[232:233], off
	s_waitcnt vmcnt(8)
	s_waitcnt lgkmcnt(0)
	s_barrier
	s_setprio 1
	s_waitcnt lgkmcnt(0)
	v_mfma_f32_16x16x32_bf16 v[126:129], v[156:159], v[188:191], v[126:129]
	v_mfma_f32_16x16x32_bf16 v[122:125], v[164:167], v[188:191], v[122:125]
	v_mfma_f32_16x16x32_bf16 v[110:113], v[156:159], v[196:199], v[110:113]
	v_mfma_f32_16x16x32_bf16 v[106:109], v[164:167], v[196:199], v[106:109]
	v_mfma_f32_16x16x32_bf16 v[94:97], v[156:159], v[204:207], v[94:97]
	v_mfma_f32_16x16x32_bf16 v[90:93], v[164:167], v[204:207], v[90:93]
	v_mfma_f32_16x16x32_bf16 v[78:81], v[156:159], v[216:219], v[78:81]
	v_mfma_f32_16x16x32_bf16 v[74:77], v[164:167], v[216:219], v[74:77]
	v_mfma_f32_16x16x32_bf16 v[126:129], v[160:163], v[192:195], v[126:129]
	v_mfma_f32_16x16x32_bf16 v[122:125], v[168:171], v[192:195], v[122:125]
	v_mfma_f32_16x16x32_bf16 v[110:113], v[160:163], v[200:203], v[110:113]
	v_mfma_f32_16x16x32_bf16 v[106:109], v[168:171], v[200:203], v[106:109]
	v_mfma_f32_16x16x32_bf16 v[94:97], v[160:163], v[212:215], v[94:97]
	v_mfma_f32_16x16x32_bf16 v[90:93], v[168:171], v[212:215], v[90:93]
	v_mfma_f32_16x16x32_bf16 v[78:81], v[160:163], v[220:223], v[78:81]
	v_mfma_f32_16x16x32_bf16 v[74:77], v[168:171], v[220:223], v[74:77]
	v_mfma_f32_16x16x32_bf16 v[118:121], v[172:175], v[188:191], v[118:121]
	v_mfma_f32_16x16x32_bf16 v[114:117], v[180:183], v[188:191], v[114:117]
	v_mfma_f32_16x16x32_bf16 v[102:105], v[172:175], v[196:199], v[102:105]
	v_mfma_f32_16x16x32_bf16 v[98:101], v[180:183], v[196:199], v[98:101]
	v_mfma_f32_16x16x32_bf16 v[86:89], v[172:175], v[204:207], v[86:89]
	v_mfma_f32_16x16x32_bf16 v[82:85], v[180:183], v[204:207], v[82:85]
	v_mfma_f32_16x16x32_bf16 v[70:73], v[172:175], v[216:219], v[70:73]
	v_mfma_f32_16x16x32_bf16 v[66:69], v[180:183], v[216:219], v[66:69]
	v_mfma_f32_16x16x32_bf16 v[118:121], v[176:179], v[192:195], v[118:121]
	v_mfma_f32_16x16x32_bf16 v[114:117], v[184:187], v[192:195], v[114:117]
	v_mfma_f32_16x16x32_bf16 v[102:105], v[176:179], v[200:203], v[102:105]
	v_mfma_f32_16x16x32_bf16 v[98:101], v[184:187], v[200:203], v[98:101]
	v_mfma_f32_16x16x32_bf16 v[86:89], v[176:179], v[212:215], v[86:89]
	v_mfma_f32_16x16x32_bf16 v[82:85], v[184:187], v[212:215], v[82:85]
	v_mfma_f32_16x16x32_bf16 v[70:73], v[176:179], v[220:223], v[70:73]
	v_mfma_f32_16x16x32_bf16 v[66:69], v[184:187], v[220:223], v[66:69]
	s_setprio 0
	s_barrier
	s_add_i32 s0, s33, s39
	v_lshl_add_u64 v[148:149], v[148:149], 0, s[22:23]
	s_mov_b32 m0, s0
	ds_read_b128 v[188:191], v154 offset:49152
	ds_read_b128 v[192:195], v154 offset:50176
	ds_read_b128 v[196:199], v154 offset:51200
	ds_read_b128 v[200:203], v154 offset:52224
	ds_read_b128 v[204:207], v154 offset:53248
	ds_read_b128 v[212:215], v154 offset:54272
	ds_read_b128 v[216:219], v154 offset:55296
	ds_read_b128 v[220:223], v154 offset:56320
	global_load_lds_dwordx4 v[148:149], off
	v_lshl_add_u64 v[148:149], v[208:209], 0, s[22:23]
	s_add_i32 m0, s0, 0x2000
	s_add_i32 s0, s63, s39
	global_load_lds_dwordx4 v[148:149], off
	v_lshl_add_u64 v[148:149], v[224:225], 0, s[22:23]
	s_mov_b32 m0, s0
	s_nop 0
	global_load_lds_dwordx4 v[148:149], off
	v_lshl_add_u64 v[148:149], v[226:227], 0, s[22:23]
	s_add_i32 m0, s0, 0x2000
	s_nop 0
	global_load_lds_dwordx4 v[148:149], off
	s_cmp_ge_i32 s61, s47
	s_cbranch_scc0 .Lkr3_b
	v_lshl_add_u64 v[148:149], v[228:229], 0, s[22:23]
	s_mov_b32 m0, s45
	s_nop 0
	global_load_lds_dwordx4 v[148:149], off
	v_lshl_add_u64 v[148:149], v[230:231], 0, s[22:23]
	s_mov_b32 m0, s46
	s_nop 0
	global_load_lds_dwordx4 v[148:149], off
; #define PG8_STAGE(bufoff, gbase, voff) do { _Pragma("unroll") for (int _i = 0; _i < 2; ++_i) \
;         __builtin_amdgcn_global_load_lds((const unsigned*)((const char*)(gbase) + (voff)[_i]), (PG8_LAS unsigned*)(lds + (bufoff) + ldsw + _i * 8192), 16, 0, 0); } while (0)
; #define PG8_LDA(dst, b, h) do { _Pragma("unroll") for (int m = 0; m < 4; ++m) { const bf16x8 f0_ = *(const PG8_LAS bf16x8*)(lds + PG8_SA(b, h) + aoff + m * 2048), f1_ = *(const PG8_LAS bf16x8*)(lds + PG8_SA(b, h) + aoff + m * 2048 + 1024); dst[m].set(f0_, f1_); } } while (0)
; #define PG8_WAIT_V(n) asm volatile("s_waitcnt vmcnt(" #n ")" ::: "memory")
; #define PG8_WAIT_L(n) asm volatile("s_waitcnt lgkmcnt(" #n ")" ::: "memory")
; #define PG8_BAR __builtin_amdgcn_s_barrier()
; #define PG8_SCHED __builtin_amdgcn_sched_barrier(0)
; template <class Epi, class Sched, bool ALIGN_EPI = false, bool SP2 = false>
; __device__ __forceinline__ void gemm_phase(PG8_LAS unsigned char* lds, const Gemm g, const Sched& S, const Epi& E) {
;     ...
;         for (int t = 0; t < nt; t += 2) {
;             if constexpr (Epi::MIDK) { if (t == (nt >> 1)) E.mid(acc, cur, wr, wc, fr, fq); }
;             const bool last = (t == nt - 2);
;             const char* a1 = cA + (size_t)(t + 1) * kstep;
;             const char* a2 = last ? nA : cA + (size_t)(t + 2) * kstep; const char* b2 = last ? nB : cB + (size_t)(t + 2) * kstep;
;             const char* a3 = a2 + kstep; const char* b3 = b2 + kstep;
;     ...
;             PG8_LDA(At, 1, 1); PG8_STAGE(PG8_SB(1, 0), b3, voffB); PG8_STAGE(PG8_SB(1, 1), b3 + hstepB, voffB); PG8_STAGE(PG8_SA(1, 0), a3, voffA);
;             PG8_WAIT_V(8); PG8_WAIT_L(0); PG8_BAR; PG8_MMA(1, 0, At, B0); PG8_MMA(1, 1, At, B1); PG8_BAR; PG8_SCHED;
.Lkr3_b:
	s_waitcnt vmcnt(6)
	s_waitcnt lgkmcnt(0)
	s_barrier
	s_setprio 1
	s_waitcnt lgkmcnt(0)
	v_mfma_f32_16x16x32_bf16 v[62:65], v[156:159], v[188:191], v[62:65]
	v_mfma_f32_16x16x32_bf16 v[58:61], v[164:167], v[188:191], v[58:61]
	v_mfma_f32_16x16x32_bf16 v[46:49], v[156:159], v[196:199], v[46:49]
	v_mfma_f32_16x16x32_bf16 v[42:45], v[164:167], v[196:199], v[42:45]
	v_mfma_f32_16x16x32_bf16 v[30:33], v[156:159], v[204:207], v[30:33]
	v_mfma_f32_16x16x32_bf16 v[26:29], v[164:167], v[204:207], v[26:29]
	v_mfma_f32_16x16x32_bf16 v[14:17], v[156:159], v[216:219], v[14:17]
	v_mfma_f32_16x16x32_bf16 v[6:9], v[164:167], v[216:219], v[6:9]
	v_mfma_f32_16x16x32_bf16 v[62:65], v[160:163], v[192:195], v[62:65]
	v_mfma_f32_16x16x32_bf16 v[58:61], v[168:171], v[192:195], v[58:61]
	v_mfma_f32_16x16x32_bf16 v[46:49], v[160:163], v[200:203], v[46:49]
	v_mfma_f32_16x16x32_bf16 v[42:45], v[168:171], v[200:203], v[42:45]
	v_mfma_f32_16x16x32_bf16 v[30:33], v[160:163], v[212:215], v[30:33]
	v_mfma_f32_16x16x32_bf16 v[26:29], v[168:171], v[212:215], v[26:29]
	v_mfma_f32_16x16x32_bf16 v[14:17], v[160:163], v[220:223], v[14:17]
	v_mfma_f32_16x16x32_bf16 v[6:9], v[168:171], v[220:223], v[6:9]
	v_mfma_f32_16x16x32_bf16 v[54:57], v[172:175], v[188:191], v[54:57]
	v_mfma_f32_16x16x32_bf16 v[50:53], v[180:183], v[188:191], v[50:53]
	v_mfma_f32_16x16x32_bf16 v[38:41], v[172:175], v[196:199], v[38:41]
	v_mfma_f32_16x16x32_bf16 v[34:37], v[180:183], v[196:199], v[34:37]
	v_mfma_f32_16x16x32_bf16 v[22:25], v[172:175], v[204:207], v[22:25]
	v_mfma_f32_16x16x32_bf16 v[18:21], v[180:183], v[204:207], v[18:21]
	v_mfma_f32_16x16x32_bf16 v[10:13], v[172:175], v[216:219], v[10:13]
	v_mfma_f32_16x16x32_bf16 v[2:5], v[180:183], v[216:219], v[2:5]
	v_mfma_f32_16x16x32_bf16 v[54:57], v[176:179], v[192:195], v[54:57]
	v_mfma_f32_16x16x32_bf16 v[50:53], v[184:187], v[192:195], v[50:53]
	v_mfma_f32_16x16x32_bf16 v[38:41], v[176:179], v[200:203], v[38:41]
	v_mfma_f32_16x16x32_bf16 v[34:37], v[184:187], v[200:203], v[34:37]
	v_mfma_f32_16x16x32_bf16 v[22:25], v[176:179], v[212:215], v[22:25]
	v_mfma_f32_16x16x32_bf16 v[18:21], v[184:187], v[212:215], v[18:21]
	v_mfma_f32_16x16x32_bf16 v[10:13], v[176:179], v[220:223], v[10:13]
	v_mfma_f32_16x16x32_bf16 v[2:5], v[184:187], v[220:223], v[2:5]
	s_setprio 0
	s_barrier
	s_add_u32 s30, s30, 0x100
	s_addc_u32 s31, s31, 0
	s_add_u32 s58, s58, 0x100
	s_addc_u32 s59, s59, 0
	s_cmp_ge_i32 s61, s47
	s_cselect_b32 s99, 0, 1
	s_mov_b32 s34, s61
	s_cbranch_scc0 .LBB0_1171

; #define PG8_STAGE(bufoff, gbase, voff) do { _Pragma("unroll") for (int _i = 0; _i < 2; ++_i) \
;         __builtin_amdgcn_global_load_lds((const unsigned*)((const char*)(gbase) + (voff)[_i]), (PG8_LAS unsigned*)(lds + (bufoff) + ldsw + _i * 8192), 16, 0, 0); } while (0)
; #define PG8_LDA(dst, b, h) do { _Pragma("unroll") for (int m = 0; m < 4; ++m) { const bf16x8 f0_ = *(const PG8_LAS bf16x8*)(lds + PG8_SA(b, h) + aoff + m * 2048), f1_ = *(const PG8_LAS bf16x8*)(lds + PG8_SA(b, h) + aoff + m * 2048 + 1024); dst[m].set(f0_, f1_); } } while (0)
; #define PG8_LDB(dst, b, h) do { _Pragma("unroll") for (int n = 0; n < 2; ++n) { const bf16x8 f0_ = *(const PG8_LAS bf16x8*)(lds + PG8_SB(b, h) + boff + n * 2048), f1_ = *(const PG8_LAS bf16x8*)(lds + PG8_SB(b, h) + boff + n * 2048 + 1024); dst[n].set(f0_, f1_); } } while (0)
; #define PG8_WAIT_V(n) asm volatile("s_waitcnt vmcnt(" #n ")" ::: "memory")
; #define PG8_WAIT_L(n) asm volatile("s_waitcnt lgkmcnt(" #n ")" ::: "memory")
; #define PG8_BAR __builtin_amdgcn_s_barrier()
; #define PG8_SCHED __builtin_amdgcn_sched_barrier(0)
; template <class Epi, class Sched, bool ALIGN_EPI = false, bool SP2 = false>
; __device__ __forceinline__ void gemm_phase(PG8_LAS unsigned char* lds, const Gemm g, const Sched& S, const Epi& E) {
;     ...
;             PG8_LDB(B0, 0, 0); PG8_LDB(B1, 0, 1); PG8_SCHED; PG8_LDA(At, 0, 0); PG8_STAGE(PG8_SA(1, 1), a1 + hstep, voffA);
;             PG8_WAIT_V(8); PG8_WAIT_L(0); PG8_BAR; PG8_MMA(0, 0, At, B0); PG8_MMA(0, 1, At, B1); PG8_BAR; PG8_SCHED;
;             PG8_LDA(At, 0, 1); PG8_STAGE(PG8_SB(0, 0), b2, voffB); PG8_STAGE(PG8_SB(0, 1), b2 + hstepB, voffB); PG8_STAGE(PG8_SA(0, 0), a2, voffA);
;             PG8_WAIT_V(8); PG8_WAIT_L(0); PG8_BAR; PG8_MMA(1, 0, At, B0); PG8_MMA(1, 1, At, B1); PG8_BAR; PG8_SCHED;
.Lkr4_a:
	v_lshl_add_u64 v[148:149], s[30:31], 0, v[140:141]
	s_add_i32 m0, s40, 0xc000
	ds_read_b128 v[188:191], v154
	ds_read_b128 v[192:195], v154 offset:1024
	ds_read_b128 v[196:199], v154 offset:2048
	ds_read_b128 v[200:203], v154 offset:3072
	ds_read_b128 v[204:207], v154 offset:4096
	ds_read_b128 v[212:215], v154 offset:5120
	ds_read_b128 v[216:219], v154 offset:6144
	ds_read_b128 v[220:223], v154 offset:7168
	global_load_lds_dwordx4 v[148:149], off
	v_lshl_add_u64 v[148:149], s[30:31], 0, v[142:143]
	s_add_i32 m0, s40, 0xe000
	s_nop 0
	global_load_lds_dwordx4 v[148:149], off
	s_waitcnt vmcnt(8)
	s_waitcnt lgkmcnt(0)
	s_barrier
	s_setprio 1
	s_waitcnt lgkmcnt(0)
	v_mfma_f32_16x16x32_bf16 v[126:129], v[156:159], v[188:191], v[126:129]
	v_mfma_f32_16x16x32_bf16 v[122:125], v[164:167], v[188:191], v[122:125]
	v_mfma_f32_16x16x32_bf16 v[110:113], v[156:159], v[196:199], v[110:113]
	v_mfma_f32_16x16x32_bf16 v[106:109], v[164:167], v[196:199], v[106:109]
	v_mfma_f32_16x16x32_bf16 v[94:97], v[156:159], v[204:207], v[94:97]
	v_mfma_f32_16x16x32_bf16 v[90:93], v[164:167], v[204:207], v[90:93]
	v_mfma_f32_16x16x32_bf16 v[78:81], v[156:159], v[216:219], v[78:81]
	v_mfma_f32_16x16x32_bf16 v[74:77], v[164:167], v[216:219], v[74:77]
	v_mfma_f32_16x16x32_bf16 v[126:129], v[160:163], v[192:195], v[126:129]
	v_mfma_f32_16x16x32_bf16 v[122:125], v[168:171], v[192:195], v[122:125]
	v_mfma_f32_16x16x32_bf16 v[110:113], v[160:163], v[200:203], v[110:113]
	v_mfma_f32_16x16x32_bf16 v[106:109], v[168:171], v[200:203], v[106:109]
	v_mfma_f32_16x16x32_bf16 v[94:97], v[160:163], v[212:215], v[94:97]
	v_mfma_f32_16x16x32_bf16 v[90:93], v[168:171], v[212:215], v[90:93]
	v_mfma_f32_16x16x32_bf16 v[78:81], v[160:163], v[220:223], v[78:81]
	v_mfma_f32_16x16x32_bf16 v[74:77], v[168:171], v[220:223], v[74:77]
	v_mfma_f32_16x16x32_bf16 v[118:121], v[172:175], v[188:191], v[118:121]
	v_mfma_f32_16x16x32_bf16 v[114:117], v[180:183], v[188:191], v[114:117]
	v_mfma_f32_16x16x32_bf16 v[102:105], v[172:175], v[196:199], v[102:105]
	v_mfma_f32_16x16x32_bf16 v[98:101], v[180:183], v[196:199], v[98:101]
	v_mfma_f32_16x16x32_bf16 v[86:89], v[172:175], v[204:207], v[86:89]
	v_mfma_f32_16x16x32_bf16 v[82:85], v[180:183], v[204:207], v[82:85]
	v_mfma_f32_16x16x32_bf16 v[70:73], v[172:175], v[216:219], v[70:73]
	v_mfma_f32_16x16x32_bf16 v[66:69], v[180:183], v[216:219], v[66:69]
	v_mfma_f32_16x16x32_bf16 v[118:121], v[176:179], v[192:195], v[118:121]
	v_mfma_f32_16x16x32_bf16 v[114:117], v[184:187], v[192:195], v[114:117]
	v_mfma_f32_16x16x32_bf16 v[102:105], v[176:179], v[200:203], v[102:105]
	v_mfma_f32_16x16x32_bf16 v[98:101], v[184:187], v[200:203], v[98:101]
	v_mfma_f32_16x16x32_bf16 v[86:89], v[176:179], v[212:215], v[86:89]
	v_mfma_f32_16x16x32_bf16 v[82:85], v[184:187], v[212:215], v[82:85]
	v_mfma_f32_16x16x32_bf16 v[70:73], v[176:179], v[220:223], v[70:73]
	v_mfma_f32_16x16x32_bf16 v[66:69], v[184:187], v[220:223], v[66:69]
	s_setprio 0
	s_barrier
	s_add_i32 s33, s52, s39
	v_lshl_add_u64 v[148:149], s[0:1], 0, v[132:133]
	s_mov_b32 m0, s33
	ds_read_b128 v[188:191], v154 offset:16384
	ds_read_b128 v[192:195], v154 offset:17408
	ds_read_b128 v[196:199], v154 offset:18432
	ds_read_b128 v[200:203], v154 offset:19456
	ds_read_b128 v[204:207], v154 offset:20480
	ds_read_b128 v[212:215], v154 offset:21504
	ds_read_b128 v[216:219], v154 offset:22528
	ds_read_b128 v[220:223], v154 offset:23552
	global_load_lds_dwordx4 v[148:149], off
	s_add_i32 m0, s33, 0x2000
	v_lshl_add_u64 v[208:209], s[0:1], 0, v[136:137]
	s_add_u32 s0, s0, s14
	s_addc_u32 s1, s1, s15
	s_add_i32 s33, s53, s39
	global_load_lds_dwordx4 v[208:209], off
	v_lshl_add_u64 v[224:225], s[0:1], 0, v[132:133]
	s_mov_b32 m0, s33
	v_lshl_add_u64 v[226:227], s[0:1], 0, v[136:137]
	global_load_lds_dwordx4 v[224:225], off
	s_add_i32 m0, s33, 0x2000
	v_lshl_add_u64 v[228:229], s[34:35], 0, v[130:131]
	global_load_lds_dwordx4 v[226:227], off
	v_lshl_add_u64 v[230:231], s[34:35], 0, v[134:135]
	s_waitcnt vmcnt(6)
	s_waitcnt lgkmcnt(0)
	s_barrier
	s_setprio 1
	s_waitcnt lgkmcnt(0)
	v_mfma_f32_16x16x32_bf16 v[62:65], v[156:159], v[188:191], v[62:65]
	v_mfma_f32_16x16x32_bf16 v[58:61], v[164:167], v[188:191], v[58:61]
	v_mfma_f32_16x16x32_bf16 v[46:49], v[156:159], v[196:199], v[46:49]
	v_mfma_f32_16x16x32_bf16 v[42:45], v[164:167], v[196:199], v[42:45]
	v_mfma_f32_16x16x32_bf16 v[30:33], v[156:159], v[204:207], v[30:33]
	v_mfma_f32_16x16x32_bf16 v[26:29], v[164:167], v[204:207], v[26:29]
	v_mfma_f32_16x16x32_bf16 v[14:17], v[156:159], v[216:219], v[14:17]
	v_mfma_f32_16x16x32_bf16 v[6:9], v[164:167], v[216:219], v[6:9]
	v_mfma_f32_16x16x32_bf16 v[62:65], v[160:163], v[192:195], v[62:65]
	v_mfma_f32_16x16x32_bf16 v[58:61], v[168:171], v[192:195], v[58:61]
	v_mfma_f32_16x16x32_bf16 v[46:49], v[160:163], v[200:203], v[46:49]
	v_mfma_f32_16x16x32_bf16 v[42:45], v[168:171], v[200:203], v[42:45]
	v_mfma_f32_16x16x32_bf16 v[30:33], v[160:163], v[212:215], v[30:33]
	v_mfma_f32_16x16x32_bf16 v[26:29], v[168:171], v[212:215], v[26:29]
	v_mfma_f32_16x16x32_bf16 v[14:17], v[160:163], v[220:223], v[14:17]
	v_mfma_f32_16x16x32_bf16 v[6:9], v[168:171], v[220:223], v[6:9]
	v_mfma_f32_16x16x32_bf16 v[54:57], v[172:175], v[188:191], v[54:57]
	v_mfma_f32_16x16x32_bf16 v[50:53], v[180:183], v[188:191], v[50:53]
	v_mfma_f32_16x16x32_bf16 v[38:41], v[172:175], v[196:199], v[38:41]
	v_mfma_f32_16x16x32_bf16 v[34:37], v[180:183], v[196:199], v[34:37]
	v_mfma_f32_16x16x32_bf16 v[22:25], v[172:175], v[204:207], v[22:25]
	v_mfma_f32_16x16x32_bf16 v[18:21], v[180:183], v[204:207], v[18:21]
	v_mfma_f32_16x16x32_bf16 v[10:13], v[172:175], v[216:219], v[10:13]
	v_mfma_f32_16x16x32_bf16 v[2:5], v[180:183], v[216:219], v[2:5]
	v_mfma_f32_16x16x32_bf16 v[54:57], v[176:179], v[192:195], v[54:57]
	v_mfma_f32_16x16x32_bf16 v[50:53], v[184:187], v[192:195], v[50:53]
	v_mfma_f32_16x16x32_bf16 v[38:41], v[176:179], v[200:203], v[38:41]
	v_mfma_f32_16x16x32_bf16 v[34:37], v[184:187], v[200:203], v[34:37]
	v_mfma_f32_16x16x32_bf16 v[22:25], v[176:179], v[212:215], v[22:25]
	v_mfma_f32_16x16x32_bf16 v[18:21], v[184:187], v[212:215], v[18:21]
	v_mfma_f32_16x16x32_bf16 v[10:13], v[176:179], v[220:223], v[10:13]
	v_mfma_f32_16x16x32_bf16 v[2:5], v[184:187], v[220:223], v[2:5]
	s_setprio 0
	s_barrier
; #define PG8_STAGE(bufoff, gbase, voff) do { _Pragma("unroll") for (int _i = 0; _i < 2; ++_i) \
;         __builtin_amdgcn_global_load_lds((const unsigned*)((const char*)(gbase) + (voff)[_i]), (PG8_LAS unsigned*)(lds + (bufoff) + ldsw + _i * 8192), 16, 0, 0); } while (0)
; #define PG8_LDA(dst, b, h) do { _Pragma("unroll") for (int m = 0; m < 4; ++m) { const bf16x8 f0_ = *(const PG8_LAS bf16x8*)(lds + PG8_SA(b, h) + aoff + m * 2048), f1_ = *(const PG8_LAS bf16x8*)(lds + PG8_SA(b, h) + aoff + m * 2048 + 1024); dst[m].set(f0_, f1_); } } while (0)
; #define PG8_LDB(dst, b, h) do { _Pragma("unroll") for (int n = 0; n < 2; ++n) { const bf16x8 f0_ = *(const PG8_LAS bf16x8*)(lds + PG8_SB(b, h) + boff + n * 2048), f1_ = *(const PG8_LAS bf16x8*)(lds + PG8_SB(b, h) + boff + n * 2048 + 1024); dst[n].set(f0_, f1_); } } while (0)
; #define PG8_WAIT_V(n) asm volatile("s_waitcnt vmcnt(" #n ")" ::: "memory")
; #define PG8_WAIT_L(n) asm volatile("s_waitcnt lgkmcnt(" #n ")" ::: "memory")
; #define PG8_BAR __builtin_amdgcn_s_barrier()
; #define PG8_SCHED __builtin_amdgcn_sched_barrier(0)
; template <class Epi, class Sched, bool ALIGN_EPI = false, bool SP2 = false>
; __device__ __forceinline__ void gemm_phase(PG8_LAS unsigned char* lds, const Gemm g, const Sched& S, const Epi& E) {
;     ...
;             PG8_WAIT_V(8); PG8_WAIT_L(0); PG8_BAR; PG8_MMA(1, 0, At, B0); PG8_MMA(1, 1, At, B1); PG8_BAR; PG8_SCHED;
;             PG8_LDB(B0, 1, 0); PG8_LDB(B1, 1, 1); PG8_SCHED; PG8_LDA(At, 1, 0); PG8_STAGE(PG8_SA(0, 1), a2 + hstep, voffA);
;             PG8_WAIT_V(8); PG8_WAIT_L(0); PG8_BAR; PG8_MMA(0, 0, At, B0); PG8_MMA(0, 1, At, B1); PG8_BAR; PG8_SCHED;
;             PG8_LDA(At, 1, 1); PG8_STAGE(PG8_SB(1, 0), b3, voffB); PG8_STAGE(PG8_SB(1, 1), b3 + hstepB, voffB); PG8_STAGE(PG8_SA(1, 0), a3, voffA);
	s_add_i32 s33, 0, 0x18000
	s_add_i32 s63, 0, 0x1c000
	v_add_u32_e32 v168, s33, v1
	v_add_u32_e32 v184, s63, v1
	ds_read_b128 v[156:159], v168
	ds_read_b128 v[160:163], v168 offset:1024
	ds_read_b128 v[164:167], v168 offset:2048
	ds_read_b128 v[168:171], v168 offset:3072
	ds_read_b128 v[172:175], v184
	ds_read_b128 v[176:179], v184 offset:1024
	ds_read_b128 v[180:183], v184 offset:2048
	ds_read_b128 v[184:187], v184 offset:3072
	s_add_u32 s0, s34, s12
	s_addc_u32 s1, s35, s13
	s_mov_b32 m0, s42
	v_lshl_add_u64 v[232:233], s[0:1], 0, v[130:131]
	ds_read_b128 v[188:191], v154 offset:32768
	ds_read_b128 v[192:195], v154 offset:33792
	ds_read_b128 v[196:199], v154 offset:34816
	ds_read_b128 v[200:203], v154 offset:35840
	ds_read_b128 v[204:207], v154 offset:36864
	ds_read_b128 v[212:215], v154 offset:37888
	ds_read_b128 v[216:219], v154 offset:38912
	ds_read_b128 v[220:223], v154 offset:39936
	s_mov_b32 m0, s40
	s_nop 0
	global_load_lds_dwordx4 v[228:229], off
	s_mov_b32 m0, s41
	s_nop 0
	global_load_lds_dwordx4 v[230:231], off
	s_mov_b32 m0, s42
	s_nop 0
	global_load_lds_dwordx4 v[232:233], off
	v_lshl_add_u64 v[232:233], s[0:1], 0, v[134:135]
	s_mov_b32 m0, s43
	s_nop 0
	global_load_lds_dwordx4 v[232:233], off
	s_waitcnt vmcnt(8)
	s_waitcnt lgkmcnt(0)
	s_barrier
	s_setprio 1
	s_waitcnt lgkmcnt(0)
	v_mfma_f32_16x16x32_bf16 v[126:129], v[156:159], v[188:191], v[126:129]
	v_mfma_f32_16x16x32_bf16 v[122:125], v[164:167], v[188:191], v[122:125]
	v_mfma_f32_16x16x32_bf16 v[110:113], v[156:159], v[196:199], v[110:113]
	v_mfma_f32_16x16x32_bf16 v[106:109], v[164:167], v[196:199], v[106:109]
	v_mfma_f32_16x16x32_bf16 v[94:97], v[156:159], v[204:207], v[94:97]
	v_mfma_f32_16x16x32_bf16 v[90:93], v[164:167], v[204:207], v[90:93]
	v_mfma_f32_16x16x32_bf16 v[78:81], v[156:159], v[216:219], v[78:81]
	v_mfma_f32_16x16x32_bf16 v[74:77], v[164:167], v[216:219], v[74:77]
	v_mfma_f32_16x16x32_bf16 v[126:129], v[160:163], v[192:195], v[126:129]
	v_mfma_f32_16x16x32_bf16 v[122:125], v[168:171], v[192:195], v[122:125]
	v_mfma_f32_16x16x32_bf16 v[110:113], v[160:163], v[200:203], v[110:113]
	v_mfma_f32_16x16x32_bf16 v[106:109], v[168:171], v[200:203], v[106:109]
	v_mfma_f32_16x16x32_bf16 v[94:97], v[160:163], v[212:215], v[94:97]
	v_mfma_f32_16x16x32_bf16 v[90:93], v[168:171], v[212:215], v[90:93]
	v_mfma_f32_16x16x32_bf16 v[78:81], v[160:163], v[220:223], v[78:81]
	v_mfma_f32_16x16x32_bf16 v[74:77], v[168:171], v[220:223], v[74:77]
	v_mfma_f32_16x16x32_bf16 v[118:121], v[172:175], v[188:191], v[118:121]
	v_mfma_f32_16x16x32_bf16 v[114:117], v[180:183], v[188:191], v[114:117]
	v_mfma_f32_16x16x32_bf16 v[102:105], v[172:175], v[196:199], v[102:105]
	v_mfma_f32_16x16x32_bf16 v[98:101], v[180:183], v[196:199], v[98:101]
	v_mfma_f32_16x16x32_bf16 v[86:89], v[172:175], v[204:207], v[86:89]
	v_mfma_f32_16x16x32_bf16 v[82:85], v[180:183], v[204:207], v[82:85]
	v_mfma_f32_16x16x32_bf16 v[70:73], v[172:175], v[216:219], v[70:73]
	v_mfma_f32_16x16x32_bf16 v[66:69], v[180:183], v[216:219], v[66:69]
	v_mfma_f32_16x16x32_bf16 v[118:121], v[176:179], v[192:195], v[118:121]
	v_mfma_f32_16x16x32_bf16 v[114:117], v[184:187], v[192:195], v[114:117]
	v_mfma_f32_16x16x32_bf16 v[102:105], v[176:179], v[200:203], v[102:105]
	v_mfma_f32_16x16x32_bf16 v[98:101], v[184:187], v[200:203], v[98:101]
	v_mfma_f32_16x16x32_bf16 v[86:89], v[176:179], v[212:215], v[86:89]
	v_mfma_f32_16x16x32_bf16 v[82:85], v[184:187], v[212:215], v[82:85]
	v_mfma_f32_16x16x32_bf16 v[70:73], v[176:179], v[220:223], v[70:73]
	v_mfma_f32_16x16x32_bf16 v[66:69], v[184:187], v[220:223], v[66:69]
	s_setprio 0
	s_barrier
	s_add_i32 s0, s33, s39
	v_lshl_add_u64 v[148:149], v[148:149], 0, s[22:23]
	s_mov_b32 m0, s0
	ds_read_b128 v[188:191], v154 offset:49152
	ds_read_b128 v[192:195], v154 offset:50176
	ds_read_b128 v[196:199], v154 offset:51200
	ds_read_b128 v[200:203], v154 offset:52224
	ds_read_b128 v[204:207], v154 offset:53248
	ds_read_b128 v[212:215], v154 offset:54272
	ds_read_b128 v[216:219], v154 offset:55296
	ds_read_b128 v[220:223], v154 offset:56320
	global_load_lds_dwordx4 v[148:149], off
	v_lshl_add_u64 v[148:149], v[208:209], 0, s[22:23]
	s_add_i32 m0, s0, 0x2000
	s_add_i32 s0, s63, s39
	global_load_lds_dwordx4 v[148:149], off
	v_lshl_add_u64 v[148:149], v[224:225], 0, s[22:23]
	s_mov_b32 m0, s0
	s_nop 0
	global_load_lds_dwordx4 v[148:149], off
	v_lshl_add_u64 v[148:149], v[226:227], 0, s[22:23]
	s_add_i32 m0, s0, 0x2000
	s_nop 0
	global_load_lds_dwordx4 v[148:149], off
	s_cmp_ge_i32 s61, s48
	s_cbranch_scc0 .Lkr4_b
	v_lshl_add_u64 v[148:149], v[228:229], 0, s[22:23]
	s_mov_b32 m0, s46
	s_nop 0
	global_load_lds_dwordx4 v[148:149], off
	v_lshl_add_u64 v[148:149], v[230:231], 0, s[22:23]
	s_mov_b32 m0, s47
	s_nop 0
	global_load_lds_dwordx4 v[148:149], off
; #define PG8_STAGE(bufoff, gbase, voff) do { _Pragma("unroll") for (int _i = 0; _i < 2; ++_i) \
;         __builtin_amdgcn_global_load_lds((const unsigned*)((const char*)(gbase) + (voff)[_i]), (PG8_LAS unsigned*)(lds + (bufoff) + ldsw + _i * 8192), 16, 0, 0); } while (0)
; #define PG8_LDA(dst, b, h) do { _Pragma("unroll") for (int m = 0; m < 4; ++m) { const bf16x8 f0_ = *(const PG8_LAS bf16x8*)(lds + PG8_SA(b, h) + aoff + m * 2048), f1_ = *(const PG8_LAS bf16x8*)(lds + PG8_SA(b, h) + aoff + m * 2048 + 1024); dst[m].set(f0_, f1_); } } while (0)
; #define PG8_WAIT_V(n) asm volatile("s_waitcnt vmcnt(" #n ")" ::: "memory")
; #define PG8_WAIT_L(n) asm volatile("s_waitcnt lgkmcnt(" #n ")" ::: "memory")
; #define PG8_BAR __builtin_amdgcn_s_barrier()
; #define PG8_SCHED __builtin_amdgcn_sched_barrier(0)
; template <class Epi, class Sched, bool ALIGN_EPI = false, bool SP2 = false>
; __device__ __forceinline__ void gemm_phase(PG8_LAS unsigned char* lds, const Gemm g, const Sched& S, const Epi& E) {
;     ...
;         for (int t = 0; t < nt; t += 2) {
;             if constexpr (Epi::MIDK) { if (t == (nt >> 1)) E.mid(acc, cur, wr, wc, fr, fq); }
;             const bool last = (t == nt - 2);
;             const char* a1 = cA + (size_t)(t + 1) * kstep;
;             const char* a2 = last ? nA : cA + (size_t)(t + 2) * kstep; const char* b2 = last ? nB : cB + (size_t)(t + 2) * kstep;
;             const char* a3 = a2 + kstep; const char* b3 = b2 + kstep;
;     ...
;             PG8_LDA(At, 1, 1); PG8_STAGE(PG8_SB(1, 0), b3, voffB); PG8_STAGE(PG8_SB(1, 1), b3 + hstepB, voffB); PG8_STAGE(PG8_SA(1, 0), a3, voffA);
;             PG8_WAIT_V(8); PG8_WAIT_L(0); PG8_BAR; PG8_MMA(1, 0, At, B0); PG8_MMA(1, 1, At, B1); PG8_BAR; PG8_SCHED;
.Lkr4_b:
	s_waitcnt vmcnt(6)
	s_waitcnt lgkmcnt(0)
	s_barrier
	s_setprio 1
	s_waitcnt lgkmcnt(0)
	v_mfma_f32_16x16x32_bf16 v[62:65], v[156:159], v[188:191], v[62:65]
	v_mfma_f32_16x16x32_bf16 v[58:61], v[164:167], v[188:191], v[58:61]
	v_mfma_f32_16x16x32_bf16 v[46:49], v[156:159], v[196:199], v[46:49]
	v_mfma_f32_16x16x32_bf16 v[42:45], v[164:167], v[196:199], v[42:45]
	v_mfma_f32_16x16x32_bf16 v[30:33], v[156:159], v[204:207], v[30:33]
	v_mfma_f32_16x16x32_bf16 v[26:29], v[164:167], v[204:207], v[26:29]
	v_mfma_f32_16x16x32_bf16 v[14:17], v[156:159], v[216:219], v[14:17]
	v_mfma_f32_16x16x32_bf16 v[6:9], v[164:167], v[216:219], v[6:9]
	v_mfma_f32_16x16x32_bf16 v[62:65], v[160:163], v[192:195], v[62:65]
	v_mfma_f32_16x16x32_bf16 v[58:61], v[168:171], v[192:195], v[58:61]
	v_mfma_f32_16x16x32_bf16 v[46:49], v[160:163], v[200:203], v[46:49]
	v_mfma_f32_16x16x32_bf16 v[42:45], v[168:171], v[200:203], v[42:45]
	v_mfma_f32_16x16x32_bf16 v[30:33], v[160:163], v[212:215], v[30:33]
	v_mfma_f32_16x16x32_bf16 v[26:29], v[168:171], v[212:215], v[26:29]
	v_mfma_f32_16x16x32_bf16 v[14:17], v[160:163], v[220:223], v[14:17]
	v_mfma_f32_16x16x32_bf16 v[6:9], v[168:171], v[220:223], v[6:9]
	v_mfma_f32_16x16x32_bf16 v[54:57], v[172:175], v[188:191], v[54:57]
	v_mfma_f32_16x16x32_bf16 v[50:53], v[180:183], v[188:191], v[50:53]
	v_mfma_f32_16x16x32_bf16 v[38:41], v[172:175], v[196:199], v[38:41]
	v_mfma_f32_16x16x32_bf16 v[34:37], v[180:183], v[196:199], v[34:37]
	v_mfma_f32_16x16x32_bf16 v[22:25], v[172:175], v[204:207], v[22:25]
	v_mfma_f32_16x16x32_bf16 v[18:21], v[180:183], v[204:207], v[18:21]
	v_mfma_f32_16x16x32_bf16 v[10:13], v[172:175], v[216:219], v[10:13]
	v_mfma_f32_16x16x32_bf16 v[2:5], v[180:183], v[216:219], v[2:5]
	v_mfma_f32_16x16x32_bf16 v[54:57], v[176:179], v[192:195], v[54:57]
	v_mfma_f32_16x16x32_bf16 v[50:53], v[184:187], v[192:195], v[50:53]
	v_mfma_f32_16x16x32_bf16 v[38:41], v[176:179], v[200:203], v[38:41]
	v_mfma_f32_16x16x32_bf16 v[34:37], v[184:187], v[200:203], v[34:37]
	v_mfma_f32_16x16x32_bf16 v[22:25], v[176:179], v[212:215], v[22:25]
	v_mfma_f32_16x16x32_bf16 v[18:21], v[184:187], v[212:215], v[18:21]
	v_mfma_f32_16x16x32_bf16 v[10:13], v[176:179], v[220:223], v[10:13]
	v_mfma_f32_16x16x32_bf16 v[2:5], v[184:187], v[220:223], v[2:5]
	s_setprio 0
	s_barrier
	s_add_u32 s30, s30, 0x100
	s_addc_u32 s31, s31, 0
	s_add_u32 s58, s58, 0x100
	s_addc_u32 s59, s59, 0
	s_cmp_ge_i32 s61, s48
	s_cselect_b32 s99, 0, 1
	s_mov_b32 s34, s61
	s_cbranch_scc0 .LBB0_1592

; #define PG8_STAGE(bufoff, gbase, voff) do { _Pragma("unroll") for (int _i = 0; _i < 2; ++_i) \
;         __builtin_amdgcn_global_load_lds((const unsigned*)((const char*)(gbase) + (voff)[_i]), (PG8_LAS unsigned*)(lds + (bufoff) + ldsw + _i * 8192), 16, 0, 0); } while (0)
; #define PG8_LDA(dst, b, h) do { _Pragma("unroll") for (int m = 0; m < 4; ++m) { const bf16x8 f0_ = *(const PG8_LAS bf16x8*)(lds + PG8_SA(b, h) + aoff + m * 2048), f1_ = *(const PG8_LAS bf16x8*)(lds + PG8_SA(b, h) + aoff + m * 2048 + 1024); dst[m].set(f0_, f1_); } } while (0)
; #define PG8_LDB(dst, b, h) do { _Pragma("unroll") for (int n = 0; n < 2; ++n) { const bf16x8 f0_ = *(const PG8_LAS bf16x8*)(lds + PG8_SB(b, h) + boff + n * 2048), f1_ = *(const PG8_LAS bf16x8*)(lds + PG8_SB(b, h) + boff + n * 2048 + 1024); dst[n].set(f0_, f1_); } } while (0)
; #define PG8_WAIT_V(n) asm volatile("s_waitcnt vmcnt(" #n ")" ::: "memory")
; #define PG8_WAIT_L(n) asm volatile("s_waitcnt lgkmcnt(" #n ")" ::: "memory")
; #define PG8_BAR __builtin_amdgcn_s_barrier()
; #define PG8_SCHED __builtin_amdgcn_sched_barrier(0)
; template <class Epi, class Sched, bool ALIGN_EPI = false, bool SP2 = false>
; __device__ __forceinline__ void gemm_phase(PG8_LAS unsigned char* lds, const Gemm g, const Sched& S, const Epi& E) {
;     ...
;             PG8_LDB(B0, 0, 0); PG8_LDB(B1, 0, 1); PG8_SCHED; PG8_LDA(At, 0, 0); PG8_STAGE(PG8_SA(1, 1), a1 + hstep, voffA);
;             PG8_WAIT_V(8); PG8_WAIT_L(0); PG8_BAR; PG8_MMA(0, 0, At, B0); PG8_MMA(0, 1, At, B1); PG8_BAR; PG8_SCHED;
;             PG8_LDA(At, 0, 1); PG8_STAGE(PG8_SB(0, 0), b2, voffB); PG8_STAGE(PG8_SB(0, 1), b2 + hstepB, voffB); PG8_STAGE(PG8_SA(0, 0), a2, voffA);
;             PG8_WAIT_V(8); PG8_WAIT_L(0); PG8_BAR; PG8_MMA(1, 0, At, B0); PG8_MMA(1, 1, At, B1); PG8_BAR; PG8_SCHED;
.Lkr5_a:
	v_lshl_add_u64 v[192:193], s[46:47], 0, v[176:177]
	s_add_i32 m0, s10, 0xc000
	ds_read_b128 v[184:187], v199
	ds_read_b128 v[188:191], v199 offset:1024
	ds_read_b128 v[212:215], v199 offset:2048
	ds_read_b128 v[216:219], v199 offset:3072
	ds_read_b128 v[220:223], v199 offset:4096
	ds_read_b128 v[224:227], v199 offset:5120
	ds_read_b128 v[228:231], v199 offset:6144
	ds_read_b128 v[232:235], v199 offset:7168
	global_load_lds_dwordx4 v[192:193], off
	v_lshl_add_u64 v[192:193], s[46:47], 0, v[178:179]
	s_add_i32 m0, s10, 0xe000
	s_nop 0
	global_load_lds_dwordx4 v[192:193], off
	s_waitcnt vmcnt(8)
	s_waitcnt lgkmcnt(0)
	s_barrier
	s_setprio 1
	s_waitcnt lgkmcnt(0)
	v_mfma_scale_f32_16x16x128_f8f6f4 v[158:161], v[18:25], v[184:191], v[158:161], v200, v201 op_sel_hi:[0,0,0]
	v_mfma_scale_f32_16x16x128_f8f6f4 v[154:157], v[26:33], v[184:191], v[154:157], v200, v201 op_sel_hi:[0,0,0]
	v_mfma_scale_f32_16x16x128_f8f6f4 v[142:145], v[18:25], v[212:219], v[142:145], v200, v201 op_sel_hi:[0,0,0]
	v_mfma_scale_f32_16x16x128_f8f6f4 v[138:141], v[26:33], v[212:219], v[138:141], v200, v201 op_sel_hi:[0,0,0]
	v_mfma_scale_f32_16x16x128_f8f6f4 v[126:129], v[18:25], v[220:227], v[126:129], v200, v201 op_sel_hi:[0,0,0]
	v_mfma_scale_f32_16x16x128_f8f6f4 v[122:125], v[26:33], v[220:227], v[122:125], v200, v201 op_sel_hi:[0,0,0]
	v_mfma_scale_f32_16x16x128_f8f6f4 v[110:113], v[18:25], v[228:235], v[110:113], v200, v201 op_sel_hi:[0,0,0]
	v_mfma_scale_f32_16x16x128_f8f6f4 v[106:109], v[26:33], v[228:235], v[106:109], v200, v201 op_sel_hi:[0,0,0]
	v_mfma_scale_f32_16x16x128_f8f6f4 v[150:153], v[2:9], v[184:191], v[150:153], v200, v201 op_sel_hi:[0,0,0]
	v_mfma_scale_f32_16x16x128_f8f6f4 v[146:149], v[10:17], v[184:191], v[146:149], v200, v201 op_sel_hi:[0,0,0]
	v_mfma_scale_f32_16x16x128_f8f6f4 v[134:137], v[2:9], v[212:219], v[134:137], v200, v201 op_sel_hi:[0,0,0]
	v_mfma_scale_f32_16x16x128_f8f6f4 v[130:133], v[10:17], v[212:219], v[130:133], v200, v201 op_sel_hi:[0,0,0]
	v_mfma_scale_f32_16x16x128_f8f6f4 v[118:121], v[2:9], v[220:227], v[118:121], v200, v201 op_sel_hi:[0,0,0]
	v_mfma_scale_f32_16x16x128_f8f6f4 v[114:117], v[10:17], v[220:227], v[114:117], v200, v201 op_sel_hi:[0,0,0]
	v_mfma_scale_f32_16x16x128_f8f6f4 v[102:105], v[2:9], v[228:235], v[102:105], v200, v201 op_sel_hi:[0,0,0]
	v_mfma_scale_f32_16x16x128_f8f6f4 v[98:101], v[10:17], v[228:235], v[98:101], v200, v201 op_sel_hi:[0,0,0]
	s_setprio 0
	s_barrier
	s_add_i32 s0, s73, s9
	v_lshl_add_u64 v[184:185], s[50:51], 0, v[164:165]
	s_mov_b32 m0, s0
	ds_read_b128 v[212:215], v199 offset:16384
	ds_read_b128 v[216:219], v199 offset:17408
	ds_read_b128 v[220:223], v199 offset:18432
	ds_read_b128 v[224:227], v199 offset:19456
	ds_read_b128 v[228:231], v199 offset:20480
	ds_read_b128 v[232:235], v199 offset:21504
	ds_read_b128 v[236:239], v199 offset:22528
	ds_read_b128 v[240:243], v199 offset:23552
	global_load_lds_dwordx4 v[184:185], off
	s_add_i32 m0, s0, 0x2000
	s_add_u32 s0, s50, s14
	v_lshl_add_u64 v[186:187], s[50:51], 0, v[168:169]
	s_addc_u32 s1, s51, s15
	s_add_i32 s33, s74, s9
	global_load_lds_dwordx4 v[186:187], off
	v_lshl_add_u64 v[188:189], s[0:1], 0, v[164:165]
	s_mov_b32 m0, s33
	v_lshl_add_u64 v[190:191], s[0:1], 0, v[168:169]
	global_load_lds_dwordx4 v[188:189], off
	s_add_i32 m0, s33, 0x2000
	v_lshl_add_u64 v[192:193], s[48:49], 0, v[162:163]
	global_load_lds_dwordx4 v[190:191], off
	v_lshl_add_u64 v[194:195], s[48:49], 0, v[166:167]
	s_waitcnt vmcnt(6)
	s_waitcnt lgkmcnt(0)
	s_barrier
	s_setprio 1
	s_waitcnt lgkmcnt(0)
	v_mfma_scale_f32_16x16x128_f8f6f4 v[94:97], v[18:25], v[212:219], v[94:97], v200, v201 op_sel_hi:[0,0,0]
	v_mfma_scale_f32_16x16x128_f8f6f4 v[90:93], v[26:33], v[212:219], v[90:93], v200, v201 op_sel_hi:[0,0,0]
	v_mfma_scale_f32_16x16x128_f8f6f4 v[78:81], v[18:25], v[220:227], v[78:81], v200, v201 op_sel_hi:[0,0,0]
	v_mfma_scale_f32_16x16x128_f8f6f4 v[74:77], v[26:33], v[220:227], v[74:77], v200, v201 op_sel_hi:[0,0,0]
	v_mfma_scale_f32_16x16x128_f8f6f4 v[62:65], v[18:25], v[228:235], v[62:65], v200, v201 op_sel_hi:[0,0,0]
	v_mfma_scale_f32_16x16x128_f8f6f4 v[58:61], v[26:33], v[228:235], v[58:61], v200, v201 op_sel_hi:[0,0,0]
	v_mfma_scale_f32_16x16x128_f8f6f4 v[46:49], v[18:25], v[236:243], v[46:49], v200, v201 op_sel_hi:[0,0,0]
	v_mfma_scale_f32_16x16x128_f8f6f4 v[42:45], v[26:33], v[236:243], v[42:45], v200, v201 op_sel_hi:[0,0,0]
	v_mfma_scale_f32_16x16x128_f8f6f4 v[86:89], v[2:9], v[212:219], v[86:89], v200, v201 op_sel_hi:[0,0,0]
	v_mfma_scale_f32_16x16x128_f8f6f4 v[82:85], v[10:17], v[212:219], v[82:85], v200, v201 op_sel_hi:[0,0,0]
	v_mfma_scale_f32_16x16x128_f8f6f4 v[70:73], v[2:9], v[220:227], v[70:73], v200, v201 op_sel_hi:[0,0,0]
	v_mfma_scale_f32_16x16x128_f8f6f4 v[66:69], v[10:17], v[220:227], v[66:69], v200, v201 op_sel_hi:[0,0,0]
	v_mfma_scale_f32_16x16x128_f8f6f4 v[54:57], v[2:9], v[228:235], v[54:57], v200, v201 op_sel_hi:[0,0,0]
	v_mfma_scale_f32_16x16x128_f8f6f4 v[50:53], v[10:17], v[228:235], v[50:53], v200, v201 op_sel_hi:[0,0,0]
	v_mfma_scale_f32_16x16x128_f8f6f4 v[38:41], v[2:9], v[236:243], v[38:41], v200, v201 op_sel_hi:[0,0,0]
	v_mfma_scale_f32_16x16x128_f8f6f4 v[34:37], v[10:17], v[236:243], v[34:37], v200, v201 op_sel_hi:[0,0,0]
	s_setprio 0
	s_barrier
; #define PG8_STAGE(bufoff, gbase, voff) do { _Pragma("unroll") for (int _i = 0; _i < 2; ++_i) \
;         __builtin_amdgcn_global_load_lds((const unsigned*)((const char*)(gbase) + (voff)[_i]), (PG8_LAS unsigned*)(lds + (bufoff) + ldsw + _i * 8192), 16, 0, 0); } while (0)
; #define PG8_LDA(dst, b, h) do { _Pragma("unroll") for (int m = 0; m < 4; ++m) { const bf16x8 f0_ = *(const PG8_LAS bf16x8*)(lds + PG8_SA(b, h) + aoff + m * 2048), f1_ = *(const PG8_LAS bf16x8*)(lds + PG8_SA(b, h) + aoff + m * 2048 + 1024); dst[m].set(f0_, f1_); } } while (0)
; #define PG8_LDB(dst, b, h) do { _Pragma("unroll") for (int n = 0; n < 2; ++n) { const bf16x8 f0_ = *(const PG8_LAS bf16x8*)(lds + PG8_SB(b, h) + boff + n * 2048), f1_ = *(const PG8_LAS bf16x8*)(lds + PG8_SB(b, h) + boff + n * 2048 + 1024); dst[n].set(f0_, f1_); } } while (0)
; #define PG8_WAIT_V(n) asm volatile("s_waitcnt vmcnt(" #n ")" ::: "memory")
; #define PG8_WAIT_L(n) asm volatile("s_waitcnt lgkmcnt(" #n ")" ::: "memory")
; #define PG8_BAR __builtin_amdgcn_s_barrier()
; #define PG8_SCHED __builtin_amdgcn_sched_barrier(0)
; template <class Epi, class Sched, bool ALIGN_EPI = false, bool SP2 = false>
; __device__ __forceinline__ void gemm_phase(PG8_LAS unsigned char* lds, const Gemm g, const Sched& S, const Epi& E) {
;     ...
;             PG8_WAIT_V(8); PG8_WAIT_L(0); PG8_BAR; PG8_MMA(1, 0, At, B0); PG8_MMA(1, 1, At, B1); PG8_BAR; PG8_SCHED;
;             PG8_LDB(B0, 1, 0); PG8_LDB(B1, 1, 1); PG8_SCHED; PG8_LDA(At, 1, 0); PG8_STAGE(PG8_SA(0, 1), a2 + hstep, voffA);
;             PG8_WAIT_V(8); PG8_WAIT_L(0); PG8_BAR; PG8_MMA(0, 0, At, B0); PG8_MMA(0, 1, At, B1); PG8_BAR; PG8_SCHED;
;             PG8_LDA(At, 1, 1); PG8_STAGE(PG8_SB(1, 0), b3, voffB); PG8_STAGE(PG8_SB(1, 1), b3 + hstepB, voffB); PG8_STAGE(PG8_SA(1, 0), a3, voffA);
;             PG8_WAIT_V(8); PG8_WAIT_L(0); PG8_BAR; PG8_MMA(1, 0, At, B0); PG8_MMA(1, 1, At, B1); PG8_BAR; PG8_SCHED;
	s_add_i32 s33, 0, 0x18000
	s_add_i32 s50, 0, 0x1c000
	v_add_u32_e32 v14, s33, v173
	v_add_u32_e32 v30, s50, v173
	ds_read_b128 v[2:5], v14
	ds_read_b128 v[6:9], v14 offset:1024
	ds_read_b128 v[10:13], v14 offset:2048
	ds_read_b128 v[14:17], v14 offset:3072
	ds_read_b128 v[18:21], v30
	ds_read_b128 v[22:25], v30 offset:1024
	ds_read_b128 v[26:29], v30 offset:2048
	ds_read_b128 v[30:33], v30 offset:3072
	s_add_u32 s0, s48, s12
	s_addc_u32 s1, s49, s13
	s_mov_b32 m0, s52
	v_lshl_add_u64 v[204:205], s[0:1], 0, v[162:163]
	ds_read_b128 v[212:215], v199 offset:32768
	ds_read_b128 v[216:219], v199 offset:33792
	ds_read_b128 v[220:223], v199 offset:34816
	ds_read_b128 v[224:227], v199 offset:35840
	ds_read_b128 v[228:231], v199 offset:36864
	ds_read_b128 v[232:235], v199 offset:37888
	ds_read_b128 v[236:239], v199 offset:38912
	ds_read_b128 v[240:243], v199 offset:39936
	s_mov_b32 m0, s10
	s_nop 0
	global_load_lds_dwordx4 v[192:193], off
	s_mov_b32 m0, s11
	s_nop 0
	global_load_lds_dwordx4 v[194:195], off
	s_mov_b32 m0, s52
	s_nop 0
	global_load_lds_dwordx4 v[204:205], off
	v_lshl_add_u64 v[204:205], s[0:1], 0, v[166:167]
	s_mov_b32 m0, s53
	s_nop 0
	global_load_lds_dwordx4 v[204:205], off
	s_waitcnt vmcnt(8)
	s_waitcnt lgkmcnt(0)
	s_barrier
	s_setprio 1
	s_waitcnt lgkmcnt(0)
	v_mfma_scale_f32_16x16x128_f8f6f4 v[158:161], v[2:9], v[212:219], v[158:161], v200, v201 op_sel_hi:[0,0,0]
	v_mfma_scale_f32_16x16x128_f8f6f4 v[154:157], v[10:17], v[212:219], v[154:157], v200, v201 op_sel_hi:[0,0,0]
	v_mfma_scale_f32_16x16x128_f8f6f4 v[142:145], v[2:9], v[220:227], v[142:145], v200, v201 op_sel_hi:[0,0,0]
	v_mfma_scale_f32_16x16x128_f8f6f4 v[138:141], v[10:17], v[220:227], v[138:141], v200, v201 op_sel_hi:[0,0,0]
	v_mfma_scale_f32_16x16x128_f8f6f4 v[126:129], v[2:9], v[228:235], v[126:129], v200, v201 op_sel_hi:[0,0,0]
	v_mfma_scale_f32_16x16x128_f8f6f4 v[122:125], v[10:17], v[228:235], v[122:125], v200, v201 op_sel_hi:[0,0,0]
	v_mfma_scale_f32_16x16x128_f8f6f4 v[110:113], v[2:9], v[236:243], v[110:113], v200, v201 op_sel_hi:[0,0,0]
	v_mfma_scale_f32_16x16x128_f8f6f4 v[106:109], v[10:17], v[236:243], v[106:109], v200, v201 op_sel_hi:[0,0,0]
	v_mfma_scale_f32_16x16x128_f8f6f4 v[150:153], v[18:25], v[212:219], v[150:153], v200, v201 op_sel_hi:[0,0,0]
	v_mfma_scale_f32_16x16x128_f8f6f4 v[146:149], v[26:33], v[212:219], v[146:149], v200, v201 op_sel_hi:[0,0,0]
	v_mfma_scale_f32_16x16x128_f8f6f4 v[134:137], v[18:25], v[220:227], v[134:137], v200, v201 op_sel_hi:[0,0,0]
	v_mfma_scale_f32_16x16x128_f8f6f4 v[130:133], v[26:33], v[220:227], v[130:133], v200, v201 op_sel_hi:[0,0,0]
	v_mfma_scale_f32_16x16x128_f8f6f4 v[118:121], v[18:25], v[228:235], v[118:121], v200, v201 op_sel_hi:[0,0,0]
	v_mfma_scale_f32_16x16x128_f8f6f4 v[114:117], v[26:33], v[228:235], v[114:117], v200, v201 op_sel_hi:[0,0,0]
	v_mfma_scale_f32_16x16x128_f8f6f4 v[102:105], v[18:25], v[236:243], v[102:105], v200, v201 op_sel_hi:[0,0,0]
	v_mfma_scale_f32_16x16x128_f8f6f4 v[98:101], v[26:33], v[236:243], v[98:101], v200, v201 op_sel_hi:[0,0,0]
	s_setprio 0
	s_barrier
	s_add_i32 s0, s33, s9
	v_lshl_add_u64 v[184:185], v[184:185], 0, s[28:29]
	s_mov_b32 m0, s0
	ds_read_b128 v[212:215], v199 offset:49152
	ds_read_b128 v[216:219], v199 offset:50176
	ds_read_b128 v[220:223], v199 offset:51200
	ds_read_b128 v[224:227], v199 offset:52224
	ds_read_b128 v[228:231], v199 offset:53248
	ds_read_b128 v[232:235], v199 offset:54272
	ds_read_b128 v[236:239], v199 offset:55296
	ds_read_b128 v[240:243], v199 offset:56320
	global_load_lds_dwordx4 v[184:185], off
	v_lshl_add_u64 v[184:185], v[186:187], 0, s[28:29]
	s_add_i32 m0, s0, 0x2000
	s_add_i32 s0, s50, s9
	global_load_lds_dwordx4 v[184:185], off
	v_lshl_add_u64 v[184:185], v[188:189], 0, s[28:29]
	s_mov_b32 m0, s0
	s_nop 0
	global_load_lds_dwordx4 v[184:185], off
	v_lshl_add_u64 v[184:185], v[190:191], 0, s[28:29]
	s_add_i32 m0, s0, 0x2000
	s_nop 0
	global_load_lds_dwordx4 v[184:185], off
	s_cmp_ge_i32 s82, s58
	s_cbranch_scc0 .Lkr5_b
	v_lshl_add_u64 v[184:185], v[192:193], 0, s[28:29]
	s_mov_b32 m0, s56
	s_nop 0
	global_load_lds_dwordx4 v[184:185], off
	v_lshl_add_u64 v[184:185], v[194:195], 0, s[28:29]
	s_mov_b32 m0, s57
	s_nop 0
	global_load_lds_dwordx4 v[184:185], off
.Lkr5_b:
	s_waitcnt vmcnt(6)
	s_waitcnt lgkmcnt(0)
	s_barrier
	s_setprio 1
	s_waitcnt lgkmcnt(0)
	v_mfma_scale_f32_16x16x128_f8f6f4 v[94:97], v[2:9], v[212:219], v[94:97], v200, v201 op_sel_hi:[0,0,0]
	v_mfma_scale_f32_16x16x128_f8f6f4 v[90:93], v[10:17], v[212:219], v[90:93], v200, v201 op_sel_hi:[0,0,0]
	v_mfma_scale_f32_16x16x128_f8f6f4 v[78:81], v[2:9], v[220:227], v[78:81], v200, v201 op_sel_hi:[0,0,0]
	v_mfma_scale_f32_16x16x128_f8f6f4 v[74:77], v[10:17], v[220:227], v[74:77], v200, v201 op_sel_hi:[0,0,0]
	v_mfma_scale_f32_16x16x128_f8f6f4 v[62:65], v[2:9], v[228:235], v[62:65], v200, v201 op_sel_hi:[0,0,0]
	v_mfma_scale_f32_16x16x128_f8f6f4 v[58:61], v[10:17], v[228:235], v[58:61], v200, v201 op_sel_hi:[0,0,0]
	v_mfma_scale_f32_16x16x128_f8f6f4 v[46:49], v[2:9], v[236:243], v[46:49], v200, v201 op_sel_hi:[0,0,0]
	v_mfma_scale_f32_16x16x128_f8f6f4 v[42:45], v[10:17], v[236:243], v[42:45], v200, v201 op_sel_hi:[0,0,0]
	v_mfma_scale_f32_16x16x128_f8f6f4 v[86:89], v[18:25], v[212:219], v[86:89], v200, v201 op_sel_hi:[0,0,0]
	v_mfma_scale_f32_16x16x128_f8f6f4 v[82:85], v[26:33], v[212:219], v[82:85], v200, v201 op_sel_hi:[0,0,0]
	v_mfma_scale_f32_16x16x128_f8f6f4 v[70:73], v[18:25], v[220:227], v[70:73], v200, v201 op_sel_hi:[0,0,0]
	v_mfma_scale_f32_16x16x128_f8f6f4 v[66:69], v[26:33], v[220:227], v[66:69], v200, v201 op_sel_hi:[0,0,0]
	v_mfma_scale_f32_16x16x128_f8f6f4 v[54:57], v[18:25], v[228:235], v[54:57], v200, v201 op_sel_hi:[0,0,0]
	v_mfma_scale_f32_16x16x128_f8f6f4 v[50:53], v[26:33], v[228:235], v[50:53], v200, v201 op_sel_hi:[0,0,0]
	v_mfma_scale_f32_16x16x128_f8f6f4 v[38:41], v[18:25], v[236:243], v[38:41], v200, v201 op_sel_hi:[0,0,0]
	v_mfma_scale_f32_16x16x128_f8f6f4 v[34:37], v[26:33], v[236:243], v[34:37], v200, v201 op_sel_hi:[0,0,0]
	s_setprio 0
	s_barrier
	s_add_u32 s46, s46, 0x100
	s_addc_u32 s47, s47, 0
	s_add_u32 s80, s80, 0x100
	s_addc_u32 s81, s81, 0
	s_cmp_ge_i32 s82, s58
	s_cselect_b32 s99, 0, 1
	s_mov_b32 s48, s82
	s_cbranch_scc0 .LBB0_1625

; #define PG8_STAGE(bufoff, gbase, voff) do { _Pragma("unroll") for (int _i = 0; _i < 2; ++_i) \
;         __builtin_amdgcn_global_load_lds((const unsigned*)((const char*)(gbase) + (voff)[_i]), (PG8_LAS unsigned*)(lds + (bufoff) + ldsw + _i * 8192), 16, 0, 0); } while (0)
; #define PG8_LDA(dst, b, h) do { _Pragma("unroll") for (int m = 0; m < 4; ++m) { const bf16x8 f0_ = *(const PG8_LAS bf16x8*)(lds + PG8_SA(b, h) + aoff + m * 2048), f1_ = *(const PG8_LAS bf16x8*)(lds + PG8_SA(b, h) + aoff + m * 2048 + 1024); dst[m].set(f0_, f1_); } } while (0)
; #define PG8_LDB(dst, b, h) do { _Pragma("unroll") for (int n = 0; n < 2; ++n) { const bf16x8 f0_ = *(const PG8_LAS bf16x8*)(lds + PG8_SB(b, h) + boff + n * 2048), f1_ = *(const PG8_LAS bf16x8*)(lds + PG8_SB(b, h) + boff + n * 2048 + 1024); dst[n].set(f0_, f1_); } } while (0)
; #define PG8_WAIT_V(n) asm volatile("s_waitcnt vmcnt(" #n ")" ::: "memory")
; #define PG8_WAIT_L(n) asm volatile("s_waitcnt lgkmcnt(" #n ")" ::: "memory")
; #define PG8_BAR __builtin_amdgcn_s_barrier()
; #define PG8_SCHED __builtin_amdgcn_sched_barrier(0)
; template <class Epi, class Sched, bool ALIGN_EPI = false, bool SP2 = false>
; __device__ __forceinline__ void gemm_phase(PG8_LAS unsigned char* lds, const Gemm g, const Sched& S, const Epi& E) {
;     ...
;             PG8_LDB(B0, 0, 0); PG8_LDB(B1, 0, 1); PG8_SCHED; PG8_LDA(At, 0, 0); PG8_STAGE(PG8_SA(1, 1), a1 + hstep, voffA);
;             PG8_WAIT_V(8); PG8_WAIT_L(0); PG8_BAR; PG8_MMA(0, 0, At, B0); PG8_MMA(0, 1, At, B1); PG8_BAR; PG8_SCHED;
;             PG8_LDA(At, 0, 1); PG8_STAGE(PG8_SB(0, 0), b2, voffB); PG8_STAGE(PG8_SB(0, 1), b2 + hstepB, voffB); PG8_STAGE(PG8_SA(0, 0), a2, voffA);
;             PG8_WAIT_V(8); PG8_WAIT_L(0); PG8_BAR; PG8_MMA(1, 0, At, B0); PG8_MMA(1, 1, At, B1); PG8_BAR; PG8_SCHED;
.Lkr6_a:
	v_lshl_add_u64 v[206:207], s[2:3], 0, v[198:199]
	s_add_i32 m0, s71, 0xc000
	ds_read_b128 v[152:155], v217
	ds_read_b128 v[156:159], v217 offset:1024
	ds_read_b128 v[168:171], v217 offset:2048
	ds_read_b128 v[172:175], v217 offset:3072
	ds_read_b128 v[176:179], v217 offset:4096
	ds_read_b128 v[180:183], v217 offset:5120
	ds_read_b128 v[226:229], v217 offset:6144
	ds_read_b128 v[230:233], v217 offset:7168
	global_load_lds_dwordx4 v[206:207], off
	v_lshl_add_u64 v[206:207], s[2:3], 0, v[200:201]
	s_add_i32 m0, s71, 0xe000
	s_nop 0
	global_load_lds_dwordx4 v[206:207], off
	s_waitcnt vmcnt(8)
	s_waitcnt lgkmcnt(0)
	s_barrier
	s_setprio 1
	s_waitcnt lgkmcnt(0)
	v_mfma_scale_f32_16x16x128_f8f6f4 v[164:167], v[16:23], v[152:159], v[164:167], v218, v219 op_sel_hi:[0,0,0]
	v_mfma_scale_f32_16x16x128_f8f6f4 v[160:163], v[24:31], v[152:159], v[160:163], v218, v219 op_sel_hi:[0,0,0]
	v_mfma_scale_f32_16x16x128_f8f6f4 v[140:143], v[16:23], v[168:175], v[140:143], v218, v219 op_sel_hi:[0,0,0]
	v_mfma_scale_f32_16x16x128_f8f6f4 v[136:139], v[24:31], v[168:175], v[136:139], v218, v219 op_sel_hi:[0,0,0]
	v_mfma_scale_f32_16x16x128_f8f6f4 v[108:111], v[16:23], v[176:183], v[108:111], v218, v219 op_sel_hi:[0,0,0]
	v_mfma_scale_f32_16x16x128_f8f6f4 v[104:107], v[24:31], v[176:183], v[104:107], v218, v219 op_sel_hi:[0,0,0]
	v_mfma_scale_f32_16x16x128_f8f6f4 v[116:119], v[16:23], v[226:233], v[116:119], v218, v219 op_sel_hi:[0,0,0]
	v_mfma_scale_f32_16x16x128_f8f6f4 v[112:115], v[24:31], v[226:233], v[112:115], v218, v219 op_sel_hi:[0,0,0]
	v_mfma_scale_f32_16x16x128_f8f6f4 v[148:151], v[0:7], v[152:159], v[148:151], v218, v219 op_sel_hi:[0,0,0]
	v_mfma_scale_f32_16x16x128_f8f6f4 v[144:147], v[8:15], v[152:159], v[144:147], v218, v219 op_sel_hi:[0,0,0]
	v_mfma_scale_f32_16x16x128_f8f6f4 v[132:135], v[0:7], v[168:175], v[132:135], v218, v219 op_sel_hi:[0,0,0]
	v_mfma_scale_f32_16x16x128_f8f6f4 v[128:131], v[8:15], v[168:175], v[128:131], v218, v219 op_sel_hi:[0,0,0]
	v_mfma_scale_f32_16x16x128_f8f6f4 v[124:127], v[0:7], v[176:183], v[124:127], v218, v219 op_sel_hi:[0,0,0]
	v_mfma_scale_f32_16x16x128_f8f6f4 v[120:123], v[8:15], v[176:183], v[120:123], v218, v219 op_sel_hi:[0,0,0]
	v_mfma_scale_f32_16x16x128_f8f6f4 v[100:103], v[0:7], v[226:233], v[100:103], v218, v219 op_sel_hi:[0,0,0]
	v_mfma_scale_f32_16x16x128_f8f6f4 v[96:99], v[8:15], v[226:233], v[96:99], v218, v219 op_sel_hi:[0,0,0]
	s_setprio 0
	s_barrier
	s_add_i32 s0, s67, s45
	v_lshl_add_u64 v[152:153], s[80:81], 0, v[186:187]
	s_mov_b32 m0, s0
	ds_read_b128 v[172:175], v217 offset:16384
	ds_read_b128 v[176:179], v217 offset:17408
	ds_read_b128 v[226:229], v217 offset:18432
	ds_read_b128 v[230:233], v217 offset:19456
	ds_read_b128 v[234:237], v217 offset:20480
	ds_read_b128 v[238:241], v217 offset:21504
	ds_read_b128 v[242:245], v217 offset:22528
	ds_read_b128 v[246:249], v217 offset:23552
	global_load_lds_dwordx4 v[152:153], off
	s_add_i32 m0, s0, 0x2000
	s_add_u32 s0, s80, s20
	v_lshl_add_u64 v[154:155], s[80:81], 0, v[190:191]
	s_addc_u32 s1, s81, s21
	s_add_i32 s33, s10, s45
	global_load_lds_dwordx4 v[154:155], off
	v_lshl_add_u64 v[156:157], s[0:1], 0, v[186:187]
	s_mov_b32 m0, s33
	v_lshl_add_u64 v[158:159], s[0:1], 0, v[190:191]
	global_load_lds_dwordx4 v[156:157], off
	s_add_i32 m0, s33, 0x2000
	v_lshl_add_u64 v[168:169], s[78:79], 0, v[184:185]
	global_load_lds_dwordx4 v[158:159], off
	v_lshl_add_u64 v[170:171], s[78:79], 0, v[188:189]
	s_waitcnt vmcnt(6)
	s_waitcnt lgkmcnt(0)
	s_barrier
	s_setprio 1
	s_waitcnt lgkmcnt(0)
	v_mfma_scale_f32_16x16x128_f8f6f4 v[92:95], v[16:23], v[172:179], v[92:95], v218, v219 op_sel_hi:[0,0,0]
	v_mfma_scale_f32_16x16x128_f8f6f4 v[88:91], v[24:31], v[172:179], v[88:91], v218, v219 op_sel_hi:[0,0,0]
	v_mfma_scale_f32_16x16x128_f8f6f4 v[76:79], v[16:23], v[226:233], v[76:79], v218, v219 op_sel_hi:[0,0,0]
	v_mfma_scale_f32_16x16x128_f8f6f4 v[72:75], v[24:31], v[226:233], v[72:75], v218, v219 op_sel_hi:[0,0,0]
	v_mfma_scale_f32_16x16x128_f8f6f4 v[60:63], v[16:23], v[234:241], v[60:63], v218, v219 op_sel_hi:[0,0,0]
	v_mfma_scale_f32_16x16x128_f8f6f4 v[56:59], v[24:31], v[234:241], v[56:59], v218, v219 op_sel_hi:[0,0,0]
	v_mfma_scale_f32_16x16x128_f8f6f4 v[44:47], v[16:23], v[242:249], v[44:47], v218, v219 op_sel_hi:[0,0,0]
	v_mfma_scale_f32_16x16x128_f8f6f4 v[40:43], v[24:31], v[242:249], v[40:43], v218, v219 op_sel_hi:[0,0,0]
	v_mfma_scale_f32_16x16x128_f8f6f4 v[84:87], v[0:7], v[172:179], v[84:87], v218, v219 op_sel_hi:[0,0,0]
	v_mfma_scale_f32_16x16x128_f8f6f4 v[80:83], v[8:15], v[172:179], v[80:83], v218, v219 op_sel_hi:[0,0,0]
	v_mfma_scale_f32_16x16x128_f8f6f4 v[68:71], v[0:7], v[226:233], v[68:71], v218, v219 op_sel_hi:[0,0,0]
	v_mfma_scale_f32_16x16x128_f8f6f4 v[64:67], v[8:15], v[226:233], v[64:67], v218, v219 op_sel_hi:[0,0,0]
	v_mfma_scale_f32_16x16x128_f8f6f4 v[52:55], v[0:7], v[234:241], v[52:55], v218, v219 op_sel_hi:[0,0,0]
	v_mfma_scale_f32_16x16x128_f8f6f4 v[48:51], v[8:15], v[234:241], v[48:51], v218, v219 op_sel_hi:[0,0,0]
	v_mfma_scale_f32_16x16x128_f8f6f4 v[36:39], v[0:7], v[242:249], v[36:39], v218, v219 op_sel_hi:[0,0,0]
	v_mfma_scale_f32_16x16x128_f8f6f4 v[32:35], v[8:15], v[242:249], v[32:35], v218, v219 op_sel_hi:[0,0,0]
	s_setprio 0
	s_barrier
; #define PG8_STAGE(bufoff, gbase, voff) do { _Pragma("unroll") for (int _i = 0; _i < 2; ++_i) \
;         __builtin_amdgcn_global_load_lds((const unsigned*)((const char*)(gbase) + (voff)[_i]), (PG8_LAS unsigned*)(lds + (bufoff) + ldsw + _i * 8192), 16, 0, 0); } while (0)
; #define PG8_LDA(dst, b, h) do { _Pragma("unroll") for (int m = 0; m < 4; ++m) { const bf16x8 f0_ = *(const PG8_LAS bf16x8*)(lds + PG8_SA(b, h) + aoff + m * 2048), f1_ = *(const PG8_LAS bf16x8*)(lds + PG8_SA(b, h) + aoff + m * 2048 + 1024); dst[m].set(f0_, f1_); } } while (0)
; #define PG8_LDB(dst, b, h) do { _Pragma("unroll") for (int n = 0; n < 2; ++n) { const bf16x8 f0_ = *(const PG8_LAS bf16x8*)(lds + PG8_SB(b, h) + boff + n * 2048), f1_ = *(const PG8_LAS bf16x8*)(lds + PG8_SB(b, h) + boff + n * 2048 + 1024); dst[n].set(f0_, f1_); } } while (0)
; #define PG8_WAIT_V(n) asm volatile("s_waitcnt vmcnt(" #n ")" ::: "memory")
; #define PG8_WAIT_L(n) asm volatile("s_waitcnt lgkmcnt(" #n ")" ::: "memory")
; #define PG8_BAR __builtin_amdgcn_s_barrier()
; #define PG8_SCHED __builtin_amdgcn_sched_barrier(0)
; template <class Epi, class Sched, bool ALIGN_EPI = false, bool SP2 = false>
; __device__ __forceinline__ void gemm_phase(PG8_LAS unsigned char* lds, const Gemm g, const Sched& S, const Epi& E) {
;     ...
;             PG8_WAIT_V(8); PG8_WAIT_L(0); PG8_BAR; PG8_MMA(1, 0, At, B0); PG8_MMA(1, 1, At, B1); PG8_BAR; PG8_SCHED;
;             PG8_LDB(B0, 1, 0); PG8_LDB(B1, 1, 1); PG8_SCHED; PG8_LDA(At, 1, 0); PG8_STAGE(PG8_SA(0, 1), a2 + hstep, voffA);
;             PG8_WAIT_V(8); PG8_WAIT_L(0); PG8_BAR; PG8_MMA(0, 0, At, B0); PG8_MMA(0, 1, At, B1); PG8_BAR; PG8_SCHED;
;             PG8_LDA(At, 1, 1); PG8_STAGE(PG8_SB(1, 0), b3, voffB); PG8_STAGE(PG8_SB(1, 1), b3 + hstepB, voffB); PG8_STAGE(PG8_SA(1, 0), a3, voffA);
;             PG8_WAIT_V(8); PG8_WAIT_L(0); PG8_BAR; PG8_MMA(1, 0, At, B0); PG8_MMA(1, 1, At, B1); PG8_BAR; PG8_SCHED;
	s_add_i32 s33, 0, 0x18000
	s_add_i32 s80, 0, 0x1c000
	v_add_u32_e32 v12, s33, v211
	v_add_u32_e32 v28, s80, v211
	ds_read_b128 v[0:3], v12
	ds_read_b128 v[4:7], v12 offset:1024
	ds_read_b128 v[8:11], v12 offset:2048
	ds_read_b128 v[12:15], v12 offset:3072
	ds_read_b128 v[16:19], v28
	ds_read_b128 v[20:23], v28 offset:1024
	ds_read_b128 v[24:27], v28 offset:2048
	ds_read_b128 v[28:31], v28 offset:3072
	s_add_u32 s0, s78, s18
	s_addc_u32 s1, s79, s19
	s_mov_b32 m0, s86
	v_lshl_add_u64 v[180:181], s[0:1], 0, v[184:185]
	ds_read_b128 v[172:175], v217 offset:32768
	ds_read_b128 v[176:179], v217 offset:33792
	ds_read_b128 v[226:229], v217 offset:34816
	ds_read_b128 v[230:233], v217 offset:35840
	ds_read_b128 v[234:237], v217 offset:36864
	ds_read_b128 v[238:241], v217 offset:37888
	ds_read_b128 v[242:245], v217 offset:38912
	ds_read_b128 v[246:249], v217 offset:39936
	s_mov_b32 m0, s71
	s_nop 0
	global_load_lds_dwordx4 v[168:169], off
	s_mov_b32 m0, s73
	s_nop 0
	global_load_lds_dwordx4 v[170:171], off
	s_mov_b32 m0, s86
	s_nop 0
	global_load_lds_dwordx4 v[180:181], off
	v_lshl_add_u64 v[180:181], s[0:1], 0, v[188:189]
	s_mov_b32 m0, s87
	s_nop 0
	global_load_lds_dwordx4 v[180:181], off
	s_waitcnt vmcnt(8)
	s_waitcnt lgkmcnt(0)
	s_barrier
	s_setprio 1
	s_waitcnt lgkmcnt(0)
	v_mfma_scale_f32_16x16x128_f8f6f4 v[164:167], v[0:7], v[172:179], v[164:167], v218, v219 op_sel_hi:[0,0,0]
	v_mfma_scale_f32_16x16x128_f8f6f4 v[160:163], v[8:15], v[172:179], v[160:163], v218, v219 op_sel_hi:[0,0,0]
	v_mfma_scale_f32_16x16x128_f8f6f4 v[140:143], v[0:7], v[226:233], v[140:143], v218, v219 op_sel_hi:[0,0,0]
	v_mfma_scale_f32_16x16x128_f8f6f4 v[136:139], v[8:15], v[226:233], v[136:139], v218, v219 op_sel_hi:[0,0,0]
	v_mfma_scale_f32_16x16x128_f8f6f4 v[108:111], v[0:7], v[234:241], v[108:111], v218, v219 op_sel_hi:[0,0,0]
	v_mfma_scale_f32_16x16x128_f8f6f4 v[104:107], v[8:15], v[234:241], v[104:107], v218, v219 op_sel_hi:[0,0,0]
	v_mfma_scale_f32_16x16x128_f8f6f4 v[116:119], v[0:7], v[242:249], v[116:119], v218, v219 op_sel_hi:[0,0,0]
	v_mfma_scale_f32_16x16x128_f8f6f4 v[112:115], v[8:15], v[242:249], v[112:115], v218, v219 op_sel_hi:[0,0,0]
	v_mfma_scale_f32_16x16x128_f8f6f4 v[148:151], v[16:23], v[172:179], v[148:151], v218, v219 op_sel_hi:[0,0,0]
	v_mfma_scale_f32_16x16x128_f8f6f4 v[144:147], v[24:31], v[172:179], v[144:147], v218, v219 op_sel_hi:[0,0,0]
	v_mfma_scale_f32_16x16x128_f8f6f4 v[132:135], v[16:23], v[226:233], v[132:135], v218, v219 op_sel_hi:[0,0,0]
	v_mfma_scale_f32_16x16x128_f8f6f4 v[128:131], v[24:31], v[226:233], v[128:131], v218, v219 op_sel_hi:[0,0,0]
	v_mfma_scale_f32_16x16x128_f8f6f4 v[124:127], v[16:23], v[234:241], v[124:127], v218, v219 op_sel_hi:[0,0,0]
	v_mfma_scale_f32_16x16x128_f8f6f4 v[120:123], v[24:31], v[234:241], v[120:123], v218, v219 op_sel_hi:[0,0,0]
	v_mfma_scale_f32_16x16x128_f8f6f4 v[100:103], v[16:23], v[242:249], v[100:103], v218, v219 op_sel_hi:[0,0,0]
	v_mfma_scale_f32_16x16x128_f8f6f4 v[96:99], v[24:31], v[242:249], v[96:99], v218, v219 op_sel_hi:[0,0,0]
	s_setprio 0
	s_barrier
	s_add_i32 s0, s33, s45
	v_lshl_add_u64 v[152:153], v[152:153], 0, s[36:37]
	s_mov_b32 m0, s0
	ds_read_b128 v[172:175], v217 offset:49152
	ds_read_b128 v[176:179], v217 offset:50176
	ds_read_b128 v[226:229], v217 offset:51200
	ds_read_b128 v[230:233], v217 offset:52224
	ds_read_b128 v[234:237], v217 offset:53248
	ds_read_b128 v[238:241], v217 offset:54272
	ds_read_b128 v[242:245], v217 offset:55296
	ds_read_b128 v[246:249], v217 offset:56320
	global_load_lds_dwordx4 v[152:153], off
	v_lshl_add_u64 v[152:153], v[154:155], 0, s[36:37]
	s_add_i32 m0, s0, 0x2000
	s_add_i32 s0, s80, s45
	global_load_lds_dwordx4 v[152:153], off
	v_lshl_add_u64 v[152:153], v[156:157], 0, s[36:37]
	s_mov_b32 m0, s0
	s_nop 0
	global_load_lds_dwordx4 v[152:153], off
	v_lshl_add_u64 v[152:153], v[158:159], 0, s[36:37]
	s_add_i32 m0, s0, 0x2000
	s_nop 0
	global_load_lds_dwordx4 v[152:153], off
	s_cmp_ge_i32 s83, s91
	s_cbranch_scc0 .Lkr6_b
	v_lshl_add_u64 v[152:153], v[168:169], 0, s[36:37]
	s_mov_b32 m0, s93
	s_nop 0
	global_load_lds_dwordx4 v[152:153], off
	v_lshl_add_u64 v[152:153], v[170:171], 0, s[36:37]
	s_mov_b32 m0, s94
	s_nop 0
	global_load_lds_dwordx4 v[152:153], off
.Lkr6_b:
	s_waitcnt vmcnt(6)
	s_waitcnt lgkmcnt(0)
	s_barrier
	s_setprio 1
	s_waitcnt lgkmcnt(0)
	v_mfma_scale_f32_16x16x128_f8f6f4 v[92:95], v[0:7], v[172:179], v[92:95], v218, v219 op_sel_hi:[0,0,0]
	v_mfma_scale_f32_16x16x128_f8f6f4 v[88:91], v[8:15], v[172:179], v[88:91], v218, v219 op_sel_hi:[0,0,0]
	v_mfma_scale_f32_16x16x128_f8f6f4 v[76:79], v[0:7], v[226:233], v[76:79], v218, v219 op_sel_hi:[0,0,0]
	v_mfma_scale_f32_16x16x128_f8f6f4 v[72:75], v[8:15], v[226:233], v[72:75], v218, v219 op_sel_hi:[0,0,0]
	v_mfma_scale_f32_16x16x128_f8f6f4 v[60:63], v[0:7], v[234:241], v[60:63], v218, v219 op_sel_hi:[0,0,0]
	v_mfma_scale_f32_16x16x128_f8f6f4 v[56:59], v[8:15], v[234:241], v[56:59], v218, v219 op_sel_hi:[0,0,0]
	v_mfma_scale_f32_16x16x128_f8f6f4 v[44:47], v[0:7], v[242:249], v[44:47], v218, v219 op_sel_hi:[0,0,0]
	v_mfma_scale_f32_16x16x128_f8f6f4 v[40:43], v[8:15], v[242:249], v[40:43], v218, v219 op_sel_hi:[0,0,0]
	v_mfma_scale_f32_16x16x128_f8f6f4 v[84:87], v[16:23], v[172:179], v[84:87], v218, v219 op_sel_hi:[0,0,0]
	v_mfma_scale_f32_16x16x128_f8f6f4 v[80:83], v[24:31], v[172:179], v[80:83], v218, v219 op_sel_hi:[0,0,0]
	v_mfma_scale_f32_16x16x128_f8f6f4 v[68:71], v[16:23], v[226:233], v[68:71], v218, v219 op_sel_hi:[0,0,0]
	v_mfma_scale_f32_16x16x128_f8f6f4 v[64:67], v[24:31], v[226:233], v[64:67], v218, v219 op_sel_hi:[0,0,0]
	v_mfma_scale_f32_16x16x128_f8f6f4 v[52:55], v[16:23], v[234:241], v[52:55], v218, v219 op_sel_hi:[0,0,0]
	v_mfma_scale_f32_16x16x128_f8f6f4 v[48:51], v[24:31], v[234:241], v[48:51], v218, v219 op_sel_hi:[0,0,0]
	v_mfma_scale_f32_16x16x128_f8f6f4 v[36:39], v[16:23], v[242:249], v[36:39], v218, v219 op_sel_hi:[0,0,0]
	v_mfma_scale_f32_16x16x128_f8f6f4 v[32:35], v[24:31], v[242:249], v[32:35], v218, v219 op_sel_hi:[0,0,0]
	s_setprio 0
	s_barrier
	s_add_u32 s2, s2, 0x100
	s_addc_u32 s3, s3, 0
	s_add_u32 s57, s57, 0x100
	s_addc_u32 s82, s82, 0
	s_cmp_ge_i32 s83, s91
	s_cselect_b32 s99, 0, 1
	s_mov_b32 s78, s83
	s_cbranch_scc0 .LBB0_1658
